# snake MFMA order plus opposite sweep direction in the directly following group (group boundary keeps the B block)
# speedup vs baseline: 1.0014x; 1.0014x over previous
.LBB0_318:
	ds_read_b128 v[26:29], v185
	ds_read_b128 v[30:33], v185 offset:1024
	ds_read_b128 v[18:21], v185 offset:2048
	ds_read_b128 v[22:25], v185 offset:3072
	ds_read_b128 v[10:13], v186
	ds_read_b128 v[14:17], v186 offset:1024
	ds_read_b128 v[2:5], v186 offset:2048
	ds_read_b128 v[6:9], v186 offset:3072
	s_add_u32 s24, s26, 0xffea8080
	s_addc_u32 s25, s27, -1
	s_cmpk_eq_i32 s58, 0x52
	s_cselect_b32 s31, s5, s25
	s_cselect_b32 s30, s4, s24
	s_cselect_b32 s29, s21, s51
	s_cselect_b32 s28, s20, s50
	v_lshl_add_u64 v[212:213], s[26:27], 0, v[166:167]
	s_add_i32 m0, s7, 0xc000
	ds_read_b128 v[174:177], v187
	ds_read_b128 v[178:181], v187 offset:1024
	ds_read_b128 v[188:191], v187 offset:2048
	ds_read_b128 v[192:195], v187 offset:3072
	ds_read_b128 v[196:199], v187 offset:4096
	ds_read_b128 v[200:203], v187 offset:5120
	ds_read_b128 v[204:207], v187 offset:6144
	ds_read_b128 v[208:211], v187 offset:7168
	global_load_lds_dwordx4 v[212:213], off
	v_lshl_add_u64 v[212:213], s[26:27], 0, v[168:169]
	s_add_i32 m0, s7, 0xe000
	s_nop 0
	global_load_lds_dwordx4 v[212:213], off
	s_waitcnt vmcnt(8)
	s_waitcnt lgkmcnt(0)
	s_barrier
	s_setprio 1
	s_waitcnt lgkmcnt(0)
	v_mfma_scale_f32_16x16x128_f8f6f4 v[158:161], v[26:33], v[174:181], v[158:161], v1, v1 op_sel_hi:[0,0,0]
	v_mfma_scale_f32_16x16x128_f8f6f4 v[154:157], v[18:25], v[174:181], v[154:157], v1, v1 op_sel_hi:[0,0,0]
	v_mfma_scale_f32_16x16x128_f8f6f4 v[138:141], v[18:25], v[188:195], v[138:141], v1, v1 op_sel_hi:[0,0,0]
	v_mfma_scale_f32_16x16x128_f8f6f4 v[142:145], v[26:33], v[188:195], v[142:145], v1, v1 op_sel_hi:[0,0,0]
	v_mfma_scale_f32_16x16x128_f8f6f4 v[126:129], v[26:33], v[196:203], v[126:129], v1, v1 op_sel_hi:[0,0,0]
	v_mfma_scale_f32_16x16x128_f8f6f4 v[122:125], v[18:25], v[196:203], v[122:125], v1, v1 op_sel_hi:[0,0,0]
	v_mfma_scale_f32_16x16x128_f8f6f4 v[106:109], v[18:25], v[204:211], v[106:109], v1, v1 op_sel_hi:[0,0,0]
	v_mfma_scale_f32_16x16x128_f8f6f4 v[110:113], v[26:33], v[204:211], v[110:113], v1, v1 op_sel_hi:[0,0,0]
	s_setprio 0
	s_setprio 1
	v_mfma_scale_f32_16x16x128_f8f6f4 v[102:105], v[10:17], v[204:211], v[102:105], v1, v1 op_sel_hi:[0,0,0]
	v_mfma_scale_f32_16x16x128_f8f6f4 v[98:101], v[2:9], v[204:211], v[98:101], v1, v1 op_sel_hi:[0,0,0]
	v_mfma_scale_f32_16x16x128_f8f6f4 v[114:117], v[2:9], v[196:203], v[114:117], v1, v1 op_sel_hi:[0,0,0]
	v_mfma_scale_f32_16x16x128_f8f6f4 v[118:121], v[10:17], v[196:203], v[118:121], v1, v1 op_sel_hi:[0,0,0]
	v_mfma_scale_f32_16x16x128_f8f6f4 v[134:137], v[10:17], v[188:195], v[134:137], v1, v1 op_sel_hi:[0,0,0]
	v_mfma_scale_f32_16x16x128_f8f6f4 v[130:133], v[2:9], v[188:195], v[130:133], v1, v1 op_sel_hi:[0,0,0]
	v_mfma_scale_f32_16x16x128_f8f6f4 v[146:149], v[2:9], v[174:181], v[146:149], v1, v1 op_sel_hi:[0,0,0]
	v_mfma_scale_f32_16x16x128_f8f6f4 v[150:153], v[10:17], v[174:181], v[150:153], v1, v1 op_sel_hi:[0,0,0]
	s_setprio 0
	s_barrier
	s_add_i32 s24, s42, s3
	v_lshl_add_u64 v[174:175], s[28:29], 0, v[164:165]
	s_mov_b32 m0, s24
	ds_read_b128 v[188:191], v187 offset:16384
	ds_read_b128 v[192:195], v187 offset:17408
	ds_read_b128 v[196:199], v187 offset:18432
	ds_read_b128 v[200:203], v187 offset:19456
	ds_read_b128 v[204:207], v187 offset:20480
	ds_read_b128 v[208:211], v187 offset:21504
	ds_read_b128 v[212:215], v187 offset:22528
	ds_read_b128 v[216:219], v187 offset:23552
	global_load_lds_dwordx4 v[174:175], off
	s_add_i32 m0, s24, 0x2000
	s_add_u32 s24, s28, 0x158000
	v_lshl_add_u64 v[176:177], s[28:29], 0, v[162:163]
	s_addc_u32 s25, s29, 0
	s_add_i32 s59, s43, s3
	global_load_lds_dwordx4 v[176:177], off
	v_lshl_add_u64 v[178:179], s[24:25], 0, v[164:165]
	s_mov_b32 m0, s59
	v_lshl_add_u64 v[180:181], s[30:31], 0, v[162:163]
	global_load_lds_dwordx4 v[178:179], off
	v_lshl_add_u64 v[178:179], s[24:25], 0, v[162:163]
	s_add_i32 m0, s59, 0x2000
	s_nop 0
	global_load_lds_dwordx4 v[178:179], off
	v_lshl_add_u64 v[178:179], s[30:31], 0, v[164:165]
	s_mov_b32 m0, s7
	s_nop 0
	global_load_lds_dwordx4 v[178:179], off
	s_mov_b32 m0, s17
	s_nop 0
	global_load_lds_dwordx4 v[180:181], off
	s_waitcnt vmcnt(8)
	s_waitcnt lgkmcnt(0)
	s_barrier
	s_setprio 1
	s_waitcnt lgkmcnt(0)
	v_mfma_scale_f32_16x16x128_f8f6f4 v[94:97], v[26:33], v[188:195], v[94:97], v1, v1 op_sel_hi:[0,0,0]
	v_mfma_scale_f32_16x16x128_f8f6f4 v[90:93], v[18:25], v[188:195], v[90:93], v1, v1 op_sel_hi:[0,0,0]
	v_mfma_scale_f32_16x16x128_f8f6f4 v[74:77], v[18:25], v[196:203], v[74:77], v1, v1 op_sel_hi:[0,0,0]
	v_mfma_scale_f32_16x16x128_f8f6f4 v[78:81], v[26:33], v[196:203], v[78:81], v1, v1 op_sel_hi:[0,0,0]
	v_mfma_scale_f32_16x16x128_f8f6f4 v[62:65], v[26:33], v[204:211], v[62:65], v1, v1 op_sel_hi:[0,0,0]
	v_mfma_scale_f32_16x16x128_f8f6f4 v[58:61], v[18:25], v[204:211], v[58:61], v1, v1 op_sel_hi:[0,0,0]
	v_mfma_scale_f32_16x16x128_f8f6f4 v[42:45], v[18:25], v[212:219], v[42:45], v1, v1 op_sel_hi:[0,0,0]
	v_mfma_scale_f32_16x16x128_f8f6f4 v[46:49], v[26:33], v[212:219], v[46:49], v1, v1 op_sel_hi:[0,0,0]
	s_setprio 0
	s_setprio 1
	v_mfma_scale_f32_16x16x128_f8f6f4 v[38:41], v[10:17], v[212:219], v[38:41], v1, v1 op_sel_hi:[0,0,0]
	v_mfma_scale_f32_16x16x128_f8f6f4 v[34:37], v[2:9], v[212:219], v[34:37], v1, v1 op_sel_hi:[0,0,0]
	v_mfma_scale_f32_16x16x128_f8f6f4 v[50:53], v[2:9], v[204:211], v[50:53], v1, v1 op_sel_hi:[0,0,0]
	v_mfma_scale_f32_16x16x128_f8f6f4 v[54:57], v[10:17], v[204:211], v[54:57], v1, v1 op_sel_hi:[0,0,0]
	v_mfma_scale_f32_16x16x128_f8f6f4 v[70:73], v[10:17], v[196:203], v[70:73], v1, v1 op_sel_hi:[0,0,0]
	v_mfma_scale_f32_16x16x128_f8f6f4 v[66:69], v[2:9], v[196:203], v[66:69], v1, v1 op_sel_hi:[0,0,0]
	v_mfma_scale_f32_16x16x128_f8f6f4 v[82:85], v[2:9], v[188:195], v[82:85], v1, v1 op_sel_hi:[0,0,0]
	v_mfma_scale_f32_16x16x128_f8f6f4 v[86:89], v[10:17], v[188:195], v[86:89], v1, v1 op_sel_hi:[0,0,0]
	s_setprio 0
	s_barrier
	s_add_i32 s59, 0, 0x18000
	s_add_i32 s60, 0, 0x1c000
	v_add_u32_e32 v14, s59, v183
	v_add_u32_e32 v30, s60, v183
	ds_read_b128 v[2:5], v14
	ds_read_b128 v[6:9], v14 offset:1024
	ds_read_b128 v[10:13], v14 offset:2048
	ds_read_b128 v[14:17], v14 offset:3072
	ds_read_b128 v[18:21], v30
	ds_read_b128 v[22:25], v30 offset:1024
	ds_read_b128 v[26:29], v30 offset:2048
	ds_read_b128 v[30:33], v30 offset:3072
	s_add_u32 s24, s30, 0x158000
	s_addc_u32 s25, s31, 0
	s_mov_b32 m0, s34
	v_lshl_add_u64 v[220:221], s[24:25], 0, v[164:165]
	ds_read_b128 v[188:191], v187 offset:32768
	ds_read_b128 v[192:195], v187 offset:33792
	ds_read_b128 v[196:199], v187 offset:34816
	ds_read_b128 v[200:203], v187 offset:35840
	ds_read_b128 v[204:207], v187 offset:36864
	ds_read_b128 v[208:211], v187 offset:37888
	ds_read_b128 v[212:215], v187 offset:38912
	ds_read_b128 v[216:219], v187 offset:39936
	global_load_lds_dwordx4 v[220:221], off
	v_lshl_add_u64 v[220:221], s[24:25], 0, v[162:163]
	s_mov_b32 m0, s35
	s_nop 0
	global_load_lds_dwordx4 v[220:221], off
	s_waitcnt vmcnt(8)
	s_waitcnt lgkmcnt(0)
	s_barrier
	s_setprio 1
	s_waitcnt lgkmcnt(0)
	v_mfma_scale_f32_16x16x128_f8f6f4 v[158:161], v[2:9], v[188:195], v[158:161], v1, v1 op_sel_hi:[0,0,0]
	v_mfma_scale_f32_16x16x128_f8f6f4 v[154:157], v[10:17], v[188:195], v[154:157], v1, v1 op_sel_hi:[0,0,0]
	v_mfma_scale_f32_16x16x128_f8f6f4 v[138:141], v[10:17], v[196:203], v[138:141], v1, v1 op_sel_hi:[0,0,0]
	v_mfma_scale_f32_16x16x128_f8f6f4 v[142:145], v[2:9], v[196:203], v[142:145], v1, v1 op_sel_hi:[0,0,0]
	v_mfma_scale_f32_16x16x128_f8f6f4 v[126:129], v[2:9], v[204:211], v[126:129], v1, v1 op_sel_hi:[0,0,0]
	v_mfma_scale_f32_16x16x128_f8f6f4 v[122:125], v[10:17], v[204:211], v[122:125], v1, v1 op_sel_hi:[0,0,0]
	v_mfma_scale_f32_16x16x128_f8f6f4 v[106:109], v[10:17], v[212:219], v[106:109], v1, v1 op_sel_hi:[0,0,0]
	v_mfma_scale_f32_16x16x128_f8f6f4 v[110:113], v[2:9], v[212:219], v[110:113], v1, v1 op_sel_hi:[0,0,0]
	s_setprio 0
	s_setprio 1
	v_mfma_scale_f32_16x16x128_f8f6f4 v[102:105], v[18:25], v[212:219], v[102:105], v1, v1 op_sel_hi:[0,0,0]
	v_mfma_scale_f32_16x16x128_f8f6f4 v[98:101], v[26:33], v[212:219], v[98:101], v1, v1 op_sel_hi:[0,0,0]
	v_mfma_scale_f32_16x16x128_f8f6f4 v[114:117], v[26:33], v[204:211], v[114:117], v1, v1 op_sel_hi:[0,0,0]
	v_mfma_scale_f32_16x16x128_f8f6f4 v[118:121], v[18:25], v[204:211], v[118:121], v1, v1 op_sel_hi:[0,0,0]
	v_mfma_scale_f32_16x16x128_f8f6f4 v[134:137], v[18:25], v[196:203], v[134:137], v1, v1 op_sel_hi:[0,0,0]
	v_mfma_scale_f32_16x16x128_f8f6f4 v[130:133], v[26:33], v[196:203], v[130:133], v1, v1 op_sel_hi:[0,0,0]
	v_mfma_scale_f32_16x16x128_f8f6f4 v[146:149], v[26:33], v[188:195], v[146:149], v1, v1 op_sel_hi:[0,0,0]
	v_mfma_scale_f32_16x16x128_f8f6f4 v[150:153], v[18:25], v[188:195], v[150:153], v1, v1 op_sel_hi:[0,0,0]
	s_setprio 0
	s_barrier
	s_add_i32 s24, s59, s3
	v_lshl_add_u64 v[174:175], v[174:175], 0, s[12:13]
	s_mov_b32 m0, s24
	ds_read_b128 v[188:191], v187 offset:49152
	ds_read_b128 v[192:195], v187 offset:50176
	ds_read_b128 v[196:199], v187 offset:51200
	ds_read_b128 v[200:203], v187 offset:52224
	ds_read_b128 v[204:207], v187 offset:53248
	ds_read_b128 v[208:211], v187 offset:54272
	ds_read_b128 v[212:215], v187 offset:55296
	ds_read_b128 v[216:219], v187 offset:56320
	global_load_lds_dwordx4 v[174:175], off
	s_add_i32 m0, s24, 0x2000
	s_add_u32 s24, s28, 0x158080
	v_lshl_add_u64 v[174:175], v[176:177], 0, s[12:13]
	s_addc_u32 s25, s29, 0
	s_add_i32 s28, s60, s3
	global_load_lds_dwordx4 v[174:175], off
	v_lshl_add_u64 v[174:175], s[24:25], 0, v[164:165]
	s_mov_b32 m0, s28
	s_nop 0
	global_load_lds_dwordx4 v[174:175], off
	v_lshl_add_u64 v[174:175], s[24:25], 0, v[162:163]
	s_add_i32 m0, s28, 0x2000
	s_nop 0
	global_load_lds_dwordx4 v[174:175], off
	v_lshl_add_u64 v[174:175], v[178:179], 0, s[12:13]
	s_mov_b32 m0, s38
	s_nop 0
	global_load_lds_dwordx4 v[174:175], off
	v_lshl_add_u64 v[174:175], v[180:181], 0, s[12:13]
	s_mov_b32 m0, s39
	s_nop 0
	global_load_lds_dwordx4 v[174:175], off
	s_waitcnt vmcnt(8)
	s_waitcnt lgkmcnt(0)
	s_barrier
	s_setprio 1
	s_waitcnt lgkmcnt(0)
	v_mfma_scale_f32_16x16x128_f8f6f4 v[94:97], v[2:9], v[188:195], v[94:97], v1, v1 op_sel_hi:[0,0,0]
	v_mfma_scale_f32_16x16x128_f8f6f4 v[90:93], v[10:17], v[188:195], v[90:93], v1, v1 op_sel_hi:[0,0,0]
	v_mfma_scale_f32_16x16x128_f8f6f4 v[74:77], v[10:17], v[196:203], v[74:77], v1, v1 op_sel_hi:[0,0,0]
	v_mfma_scale_f32_16x16x128_f8f6f4 v[78:81], v[2:9], v[196:203], v[78:81], v1, v1 op_sel_hi:[0,0,0]
	v_mfma_scale_f32_16x16x128_f8f6f4 v[62:65], v[2:9], v[204:211], v[62:65], v1, v1 op_sel_hi:[0,0,0]
	v_mfma_scale_f32_16x16x128_f8f6f4 v[58:61], v[10:17], v[204:211], v[58:61], v1, v1 op_sel_hi:[0,0,0]
	v_mfma_scale_f32_16x16x128_f8f6f4 v[42:45], v[10:17], v[212:219], v[42:45], v1, v1 op_sel_hi:[0,0,0]
	v_mfma_scale_f32_16x16x128_f8f6f4 v[46:49], v[2:9], v[212:219], v[46:49], v1, v1 op_sel_hi:[0,0,0]
	s_setprio 0
	s_setprio 1
	v_mfma_scale_f32_16x16x128_f8f6f4 v[38:41], v[18:25], v[212:219], v[38:41], v1, v1 op_sel_hi:[0,0,0]
	v_mfma_scale_f32_16x16x128_f8f6f4 v[34:37], v[26:33], v[212:219], v[34:37], v1, v1 op_sel_hi:[0,0,0]
	v_mfma_scale_f32_16x16x128_f8f6f4 v[50:53], v[26:33], v[204:211], v[50:53], v1, v1 op_sel_hi:[0,0,0]
	v_mfma_scale_f32_16x16x128_f8f6f4 v[54:57], v[18:25], v[204:211], v[54:57], v1, v1 op_sel_hi:[0,0,0]
	v_mfma_scale_f32_16x16x128_f8f6f4 v[70:73], v[18:25], v[196:203], v[70:73], v1, v1 op_sel_hi:[0,0,0]
	v_mfma_scale_f32_16x16x128_f8f6f4 v[66:69], v[26:33], v[196:203], v[66:69], v1, v1 op_sel_hi:[0,0,0]
	v_mfma_scale_f32_16x16x128_f8f6f4 v[82:85], v[26:33], v[188:195], v[82:85], v1, v1 op_sel_hi:[0,0,0]
	v_mfma_scale_f32_16x16x128_f8f6f4 v[86:89], v[18:25], v[188:195], v[86:89], v1, v1 op_sel_hi:[0,0,0]
	s_setprio 0
	s_barrier
	s_add_i32 s58, s58, 2
	s_add_u32 s26, s26, 0x100
	s_addc_u32 s27, s27, 0
	s_add_u32 s50, s50, 0x100
	s_addc_u32 s51, s51, 0
	s_cmpk_gt_u32 s58, 0x53
	s_cbranch_scc0 .LBB0_318
	s_and_b64 vcc, exec, s[14:15]
	s_cbranch_vccz .LBB0_321
	s_barrier

.LBB0_332:
	s_add_u32 s6, s61, s4
	s_addc_u32 s7, s62, s5
	s_add_u32 s6, s6, 0x32800100
	s_addc_u32 s7, s7, 0
	s_add_u32 s24, s63, s4
	s_addc_u32 s25, s68, s5
	s_add_i32 s64, 0, 0x10000
	s_cmpk_eq_i32 s4, 0x2a00
	s_cselect_b32 s13, s1, s7
	s_cselect_b32 s12, s0, s6
	s_cselect_b32 s7, s29, s25
	s_cselect_b32 s6, s28, s24
	s_add_i32 s65, 0, 0x14000
	v_add_u32_e32 v2, s64, v188
	v_add_u32_e32 v6, s65, v188
	ds_read_b128 v[26:29], v2
	ds_read_b128 v[30:33], v2 offset:1024
	ds_read_b128 v[18:21], v2 offset:2048
	ds_read_b128 v[22:25], v2 offset:3072
	ds_read_b128 v[10:13], v6
	ds_read_b128 v[14:17], v6 offset:1024
	ds_read_b128 v[2:5], v6 offset:2048
	ds_read_b128 v[6:9], v6 offset:3072
	v_lshl_add_u64 v[214:215], v[168:169], 0, s[4:5]
	s_add_i32 m0, s18, 0xc000
	ds_read_b128 v[172:175], v189
	ds_read_b128 v[176:179], v189 offset:1024
	ds_read_b128 v[190:193], v189 offset:2048
	ds_read_b128 v[194:197], v189 offset:3072
	ds_read_b128 v[198:201], v189 offset:4096
	ds_read_b128 v[202:205], v189 offset:5120
	ds_read_b128 v[206:209], v189 offset:6144
	ds_read_b128 v[210:213], v189 offset:7168
	global_load_lds_dwordx4 v[214:215], off
	v_lshl_add_u64 v[214:215], v[170:171], 0, s[4:5]
	s_add_i32 m0, s18, 0xe000
	s_nop 0
	global_load_lds_dwordx4 v[214:215], off
	s_waitcnt vmcnt(8)
	s_waitcnt lgkmcnt(0)
	s_barrier
	s_setprio 1
	s_waitcnt lgkmcnt(0)
	v_mfma_scale_f32_16x16x128_f8f6f4 v[70:73], v[26:33], v[172:179], v[70:73], v187, v187 op_sel_hi:[0,0,0]
	v_mfma_scale_f32_16x16x128_f8f6f4 v[66:69], v[18:25], v[172:179], v[66:69], v187, v187 op_sel_hi:[0,0,0]
	v_mfma_scale_f32_16x16x128_f8f6f4 v[74:77], v[18:25], v[190:197], v[74:77], v187, v187 op_sel_hi:[0,0,0]
	v_mfma_scale_f32_16x16x128_f8f6f4 v[78:81], v[26:33], v[190:197], v[78:81], v187, v187 op_sel_hi:[0,0,0]
	v_mfma_scale_f32_16x16x128_f8f6f4 v[86:89], v[26:33], v[198:205], v[86:89], v187, v187 op_sel_hi:[0,0,0]
	v_mfma_scale_f32_16x16x128_f8f6f4 v[82:85], v[18:25], v[198:205], v[82:85], v187, v187 op_sel_hi:[0,0,0]
	v_mfma_scale_f32_16x16x128_f8f6f4 v[90:93], v[18:25], v[206:213], v[90:93], v187, v187 op_sel_hi:[0,0,0]
	v_mfma_scale_f32_16x16x128_f8f6f4 v[94:97], v[26:33], v[206:213], v[94:97], v187, v187 op_sel_hi:[0,0,0]
	s_setprio 0
	s_setprio 1
	v_mfma_scale_f32_16x16x128_f8f6f4 v[134:137], v[10:17], v[206:213], v[134:137], v187, v187 op_sel_hi:[0,0,0]
	v_mfma_scale_f32_16x16x128_f8f6f4 v[130:133], v[2:9], v[206:213], v[130:133], v187, v187 op_sel_hi:[0,0,0]
	v_mfma_scale_f32_16x16x128_f8f6f4 v[138:141], v[2:9], v[198:205], v[138:141], v187, v187 op_sel_hi:[0,0,0]
	v_mfma_scale_f32_16x16x128_f8f6f4 v[142:145], v[10:17], v[198:205], v[142:145], v187, v187 op_sel_hi:[0,0,0]
	v_mfma_scale_f32_16x16x128_f8f6f4 v[150:153], v[10:17], v[190:197], v[150:153], v187, v187 op_sel_hi:[0,0,0]
	v_mfma_scale_f32_16x16x128_f8f6f4 v[146:149], v[2:9], v[190:197], v[146:149], v187, v187 op_sel_hi:[0,0,0]
	v_mfma_scale_f32_16x16x128_f8f6f4 v[154:157], v[2:9], v[172:179], v[154:157], v187, v187 op_sel_hi:[0,0,0]
	v_mfma_scale_f32_16x16x128_f8f6f4 v[158:161], v[10:17], v[172:179], v[158:161], v187, v187 op_sel_hi:[0,0,0]
	s_setprio 0
	s_barrier
	s_add_i32 s24, s64, s17
	v_lshl_add_u64 v[172:173], s[6:7], 0, v[162:163]
	s_mov_b32 m0, s24
	ds_read_b128 v[190:193], v189 offset:16384
	ds_read_b128 v[194:197], v189 offset:17408
	ds_read_b128 v[198:201], v189 offset:18432
	ds_read_b128 v[202:205], v189 offset:19456
	ds_read_b128 v[206:209], v189 offset:20480
	ds_read_b128 v[210:213], v189 offset:21504
	ds_read_b128 v[214:217], v189 offset:22528
	ds_read_b128 v[218:221], v189 offset:23552
	global_load_lds_dwordx4 v[172:173], off
	s_add_i32 m0, s24, 0x2000
	s_add_u32 s24, s6, 0x158000
	v_lshl_add_u64 v[174:175], s[6:7], 0, v[166:167]
	s_addc_u32 s25, s7, 0
	s_add_i32 s64, s65, s17
	global_load_lds_dwordx4 v[174:175], off
	v_lshl_add_u64 v[176:177], s[24:25], 0, v[162:163]
	s_mov_b32 m0, s64
	v_lshl_add_u64 v[178:179], s[12:13], 0, v[166:167]
	global_load_lds_dwordx4 v[176:177], off
	v_lshl_add_u64 v[176:177], s[24:25], 0, v[166:167]
	s_add_i32 m0, s64, 0x2000
	s_nop 0
	global_load_lds_dwordx4 v[176:177], off
	v_lshl_add_u64 v[176:177], s[12:13], 0, v[162:163]
	s_mov_b32 m0, s18
	s_nop 0
	global_load_lds_dwordx4 v[176:177], off
	s_mov_b32 m0, s19
	s_nop 0
	global_load_lds_dwordx4 v[178:179], off
	s_waitcnt vmcnt(8)
	s_waitcnt lgkmcnt(0)
	s_barrier
	s_setprio 1
	s_waitcnt lgkmcnt(0)
	v_mfma_scale_f32_16x16x128_f8f6f4 v[102:105], v[26:33], v[190:197], v[102:105], v187, v187 op_sel_hi:[0,0,0]
	v_mfma_scale_f32_16x16x128_f8f6f4 v[98:101], v[18:25], v[190:197], v[98:101], v187, v187 op_sel_hi:[0,0,0]
	v_mfma_scale_f32_16x16x128_f8f6f4 v[106:109], v[18:25], v[198:205], v[106:109], v187, v187 op_sel_hi:[0,0,0]
	v_mfma_scale_f32_16x16x128_f8f6f4 v[110:113], v[26:33], v[198:205], v[110:113], v187, v187 op_sel_hi:[0,0,0]
	v_mfma_scale_f32_16x16x128_f8f6f4 v[118:121], v[26:33], v[206:213], v[118:121], v187, v187 op_sel_hi:[0,0,0]
	v_mfma_scale_f32_16x16x128_f8f6f4 v[114:117], v[18:25], v[206:213], v[114:117], v187, v187 op_sel_hi:[0,0,0]
	v_mfma_scale_f32_16x16x128_f8f6f4 v[122:125], v[18:25], v[214:221], v[122:125], v187, v187 op_sel_hi:[0,0,0]
	v_mfma_scale_f32_16x16x128_f8f6f4 v[126:129], v[26:33], v[214:221], v[126:129], v187, v187 op_sel_hi:[0,0,0]
	s_setprio 0
	s_setprio 1
	v_mfma_scale_f32_16x16x128_f8f6f4 v[62:65], v[10:17], v[214:221], v[62:65], v187, v187 op_sel_hi:[0,0,0]
	v_mfma_scale_f32_16x16x128_f8f6f4 v[58:61], v[2:9], v[214:221], v[58:61], v187, v187 op_sel_hi:[0,0,0]
	v_mfma_scale_f32_16x16x128_f8f6f4 v[50:53], v[2:9], v[206:213], v[50:53], v187, v187 op_sel_hi:[0,0,0]
	v_mfma_scale_f32_16x16x128_f8f6f4 v[54:57], v[10:17], v[206:213], v[54:57], v187, v187 op_sel_hi:[0,0,0]
	v_mfma_scale_f32_16x16x128_f8f6f4 v[46:49], v[10:17], v[198:205], v[46:49], v187, v187 op_sel_hi:[0,0,0]
	v_mfma_scale_f32_16x16x128_f8f6f4 v[42:45], v[2:9], v[198:205], v[42:45], v187, v187 op_sel_hi:[0,0,0]
	v_mfma_scale_f32_16x16x128_f8f6f4 v[34:37], v[2:9], v[190:197], v[34:37], v187, v187 op_sel_hi:[0,0,0]
	v_mfma_scale_f32_16x16x128_f8f6f4 v[38:41], v[10:17], v[190:197], v[38:41], v187, v187 op_sel_hi:[0,0,0]
	s_setprio 0
	s_barrier
	s_add_i32 s24, 0, 0x18000
	s_add_i32 s25, 0, 0x1c000
	v_add_u32_e32 v14, s24, v188
	v_add_u32_e32 v30, s25, v188
	ds_read_b128 v[2:5], v14
	ds_read_b128 v[6:9], v14 offset:1024
	ds_read_b128 v[10:13], v14 offset:2048
	ds_read_b128 v[14:17], v14 offset:3072
	ds_read_b128 v[18:21], v30
	ds_read_b128 v[22:25], v30 offset:1024
	ds_read_b128 v[26:29], v30 offset:2048
	ds_read_b128 v[30:33], v30 offset:3072
	s_add_u32 s12, s12, 0x158000
	s_addc_u32 s13, s13, 0
	s_mov_b32 m0, s93
	v_lshl_add_u64 v[222:223], s[12:13], 0, v[162:163]
	ds_read_b128 v[190:193], v189 offset:32768
	ds_read_b128 v[194:197], v189 offset:33792
	ds_read_b128 v[198:201], v189 offset:34816
	ds_read_b128 v[202:205], v189 offset:35840
	ds_read_b128 v[206:209], v189 offset:36864
	ds_read_b128 v[210:213], v189 offset:37888
	ds_read_b128 v[214:217], v189 offset:38912
	ds_read_b128 v[218:221], v189 offset:39936
	global_load_lds_dwordx4 v[222:223], off
	v_lshl_add_u64 v[222:223], s[12:13], 0, v[166:167]
	s_mov_b32 m0, s94
	s_nop 0
	global_load_lds_dwordx4 v[222:223], off
	s_waitcnt vmcnt(8)
	s_waitcnt lgkmcnt(0)
	s_barrier
	s_setprio 1
	s_waitcnt lgkmcnt(0)
	v_mfma_scale_f32_16x16x128_f8f6f4 v[70:73], v[2:9], v[190:197], v[70:73], v187, v187 op_sel_hi:[0,0,0]
	v_mfma_scale_f32_16x16x128_f8f6f4 v[66:69], v[10:17], v[190:197], v[66:69], v187, v187 op_sel_hi:[0,0,0]
	v_mfma_scale_f32_16x16x128_f8f6f4 v[74:77], v[10:17], v[198:205], v[74:77], v187, v187 op_sel_hi:[0,0,0]
	v_mfma_scale_f32_16x16x128_f8f6f4 v[78:81], v[2:9], v[198:205], v[78:81], v187, v187 op_sel_hi:[0,0,0]
	v_mfma_scale_f32_16x16x128_f8f6f4 v[86:89], v[2:9], v[206:213], v[86:89], v187, v187 op_sel_hi:[0,0,0]
	v_mfma_scale_f32_16x16x128_f8f6f4 v[82:85], v[10:17], v[206:213], v[82:85], v187, v187 op_sel_hi:[0,0,0]
	v_mfma_scale_f32_16x16x128_f8f6f4 v[90:93], v[10:17], v[214:221], v[90:93], v187, v187 op_sel_hi:[0,0,0]
	v_mfma_scale_f32_16x16x128_f8f6f4 v[94:97], v[2:9], v[214:221], v[94:97], v187, v187 op_sel_hi:[0,0,0]
	s_setprio 0
	s_setprio 1
	v_mfma_scale_f32_16x16x128_f8f6f4 v[134:137], v[18:25], v[214:221], v[134:137], v187, v187 op_sel_hi:[0,0,0]
	v_mfma_scale_f32_16x16x128_f8f6f4 v[130:133], v[26:33], v[214:221], v[130:133], v187, v187 op_sel_hi:[0,0,0]
	v_mfma_scale_f32_16x16x128_f8f6f4 v[138:141], v[26:33], v[206:213], v[138:141], v187, v187 op_sel_hi:[0,0,0]
	v_mfma_scale_f32_16x16x128_f8f6f4 v[142:145], v[18:25], v[206:213], v[142:145], v187, v187 op_sel_hi:[0,0,0]
	v_mfma_scale_f32_16x16x128_f8f6f4 v[150:153], v[18:25], v[198:205], v[150:153], v187, v187 op_sel_hi:[0,0,0]
	v_mfma_scale_f32_16x16x128_f8f6f4 v[146:149], v[26:33], v[198:205], v[146:149], v187, v187 op_sel_hi:[0,0,0]
	v_mfma_scale_f32_16x16x128_f8f6f4 v[154:157], v[26:33], v[190:197], v[154:157], v187, v187 op_sel_hi:[0,0,0]
	v_mfma_scale_f32_16x16x128_f8f6f4 v[158:161], v[18:25], v[190:197], v[158:161], v187, v187 op_sel_hi:[0,0,0]
	s_setprio 0
	s_barrier
	s_add_i32 s12, s24, s17
	v_lshl_add_u64 v[172:173], v[172:173], 0, s[76:77]
	s_mov_b32 m0, s12
	ds_read_b128 v[190:193], v189 offset:49152
	ds_read_b128 v[194:197], v189 offset:50176
	ds_read_b128 v[198:201], v189 offset:51200
	ds_read_b128 v[202:205], v189 offset:52224
	ds_read_b128 v[206:209], v189 offset:53248
	ds_read_b128 v[210:213], v189 offset:54272
	ds_read_b128 v[214:217], v189 offset:55296
	ds_read_b128 v[218:221], v189 offset:56320
	global_load_lds_dwordx4 v[172:173], off
	s_add_i32 m0, s12, 0x2000
	s_add_u32 s6, s6, 0x158080
	v_lshl_add_u64 v[172:173], v[174:175], 0, s[76:77]
	s_addc_u32 s7, s7, 0
	s_add_i32 s12, s25, s17
	global_load_lds_dwordx4 v[172:173], off
	v_lshl_add_u64 v[172:173], s[6:7], 0, v[162:163]
	s_mov_b32 m0, s12
	s_nop 0
	global_load_lds_dwordx4 v[172:173], off
	v_lshl_add_u64 v[172:173], s[6:7], 0, v[166:167]
	s_add_i32 m0, s12, 0x2000
	s_nop 0
	global_load_lds_dwordx4 v[172:173], off
	v_lshl_add_u64 v[172:173], v[176:177], 0, s[76:77]
	s_mov_b32 m0, s95
	s_nop 0
	global_load_lds_dwordx4 v[172:173], off
	v_lshl_add_u64 v[172:173], v[178:179], 0, s[76:77]
	s_mov_b32 m0, vcc_lo
	s_nop 0
	global_load_lds_dwordx4 v[172:173], off
	s_waitcnt vmcnt(8)
	s_waitcnt lgkmcnt(0)
	s_barrier
	s_setprio 1
	s_waitcnt lgkmcnt(0)
	v_mfma_scale_f32_16x16x128_f8f6f4 v[102:105], v[2:9], v[190:197], v[102:105], v187, v187 op_sel_hi:[0,0,0]
	v_mfma_scale_f32_16x16x128_f8f6f4 v[98:101], v[10:17], v[190:197], v[98:101], v187, v187 op_sel_hi:[0,0,0]
	v_mfma_scale_f32_16x16x128_f8f6f4 v[106:109], v[10:17], v[198:205], v[106:109], v187, v187 op_sel_hi:[0,0,0]
	v_mfma_scale_f32_16x16x128_f8f6f4 v[110:113], v[2:9], v[198:205], v[110:113], v187, v187 op_sel_hi:[0,0,0]
	v_mfma_scale_f32_16x16x128_f8f6f4 v[118:121], v[2:9], v[206:213], v[118:121], v187, v187 op_sel_hi:[0,0,0]
	v_mfma_scale_f32_16x16x128_f8f6f4 v[114:117], v[10:17], v[206:213], v[114:117], v187, v187 op_sel_hi:[0,0,0]
	v_mfma_scale_f32_16x16x128_f8f6f4 v[122:125], v[10:17], v[214:221], v[122:125], v187, v187 op_sel_hi:[0,0,0]
	v_mfma_scale_f32_16x16x128_f8f6f4 v[126:129], v[2:9], v[214:221], v[126:129], v187, v187 op_sel_hi:[0,0,0]
	s_setprio 0
	s_setprio 1
	v_mfma_scale_f32_16x16x128_f8f6f4 v[62:65], v[18:25], v[214:221], v[62:65], v187, v187 op_sel_hi:[0,0,0]
	v_mfma_scale_f32_16x16x128_f8f6f4 v[58:61], v[26:33], v[214:221], v[58:61], v187, v187 op_sel_hi:[0,0,0]
	v_mfma_scale_f32_16x16x128_f8f6f4 v[50:53], v[26:33], v[206:213], v[50:53], v187, v187 op_sel_hi:[0,0,0]
	v_mfma_scale_f32_16x16x128_f8f6f4 v[54:57], v[18:25], v[206:213], v[54:57], v187, v187 op_sel_hi:[0,0,0]
	v_mfma_scale_f32_16x16x128_f8f6f4 v[46:49], v[18:25], v[198:205], v[46:49], v187, v187 op_sel_hi:[0,0,0]
	v_mfma_scale_f32_16x16x128_f8f6f4 v[42:45], v[26:33], v[198:205], v[42:45], v187, v187 op_sel_hi:[0,0,0]
	v_mfma_scale_f32_16x16x128_f8f6f4 v[34:37], v[26:33], v[190:197], v[34:37], v187, v187 op_sel_hi:[0,0,0]
	v_mfma_scale_f32_16x16x128_f8f6f4 v[38:41], v[18:25], v[190:197], v[38:41], v187, v187 op_sel_hi:[0,0,0]
	s_setprio 0
	s_barrier
	s_add_i32 vcc_hi, vcc_hi, 2
	s_add_u32 s4, s4, 0x100
	s_addc_u32 s5, s5, 0
	s_cmpk_lt_u32 vcc_hi, 0x54
	s_cbranch_scc1 .LBB0_332
	s_waitcnt vmcnt(0)
	s_mov_b64 s[12:13], s[54:55]
	s_cmpk_gt_u32 s89, 0xff
	s_cbranch_scc1 .LBB0_335
	s_barrier

.LBB0_1291:
	ds_read_b128 v[26:29], v184
	ds_read_b128 v[30:33], v184 offset:1024
	ds_read_b128 v[18:21], v184 offset:2048
	ds_read_b128 v[22:25], v184 offset:3072
	ds_read_b128 v[10:13], v185
	ds_read_b128 v[14:17], v185 offset:1024
	ds_read_b128 v[2:5], v185 offset:2048
	ds_read_b128 v[6:9], v185 offset:3072
	s_add_u32 s20, s14, s16
	s_addc_u32 s21, s15, s17
	s_add_u32 s20, s20, 0x2a800100
	s_addc_u32 s21, s21, 0
	s_add_u32 s48, s31, s16
	s_addc_u32 s49, s34, s17
	s_cmpk_eq_i32 s16, 0x700
	s_cselect_b32 s23, s9, s21
	s_cselect_b32 s22, s8, s20
	s_cselect_b32 s21, s5, s49
	s_cselect_b32 s20, s4, s48
	s_mov_b32 m0, s36
	v_lshl_add_u64 v[214:215], v[170:171], 0, s[16:17]
	ds_read_b128 v[174:177], v186
	ds_read_b128 v[178:181], v186 offset:1024
	ds_read_b128 v[190:193], v186 offset:2048
	ds_read_b128 v[194:197], v186 offset:3072
	ds_read_b128 v[198:201], v186 offset:4096
	ds_read_b128 v[202:205], v186 offset:5120
	ds_read_b128 v[206:209], v186 offset:6144
	ds_read_b128 v[210:213], v186 offset:7168
	global_load_lds_dwordx4 v[214:215], off
	v_lshl_add_u64 v[214:215], v[172:173], 0, s[16:17]
	s_mov_b32 m0, s37
	s_nop 0
	global_load_lds_dwordx4 v[214:215], off
	s_waitcnt vmcnt(8)
	s_waitcnt lgkmcnt(0)
	s_barrier
	s_setprio 1
	s_waitcnt lgkmcnt(0)
	v_mfma_scale_f32_16x16x128_f8f6f4 v[158:161], v[26:33], v[174:181], v[158:161], v1, v1 op_sel_hi:[0,0,0]
	v_mfma_scale_f32_16x16x128_f8f6f4 v[154:157], v[18:25], v[174:181], v[154:157], v1, v1 op_sel_hi:[0,0,0]
	v_mfma_scale_f32_16x16x128_f8f6f4 v[138:141], v[18:25], v[190:197], v[138:141], v1, v1 op_sel_hi:[0,0,0]
	v_mfma_scale_f32_16x16x128_f8f6f4 v[146:149], v[26:33], v[190:197], v[146:149], v1, v1 op_sel_hi:[0,0,0]
	v_mfma_scale_f32_16x16x128_f8f6f4 v[130:133], v[26:33], v[198:205], v[130:133], v1, v1 op_sel_hi:[0,0,0]
	v_mfma_scale_f32_16x16x128_f8f6f4 v[122:125], v[18:25], v[198:205], v[122:125], v1, v1 op_sel_hi:[0,0,0]
	v_mfma_scale_f32_16x16x128_f8f6f4 v[106:109], v[18:25], v[206:213], v[106:109], v1, v1 op_sel_hi:[0,0,0]
	v_mfma_scale_f32_16x16x128_f8f6f4 v[114:117], v[26:33], v[206:213], v[114:117], v1, v1 op_sel_hi:[0,0,0]
	s_setprio 0
	s_setprio 1
	v_mfma_scale_f32_16x16x128_f8f6f4 v[102:105], v[10:17], v[206:213], v[102:105], v1, v1 op_sel_hi:[0,0,0]
	v_mfma_scale_f32_16x16x128_f8f6f4 v[98:101], v[2:9], v[206:213], v[98:101], v1, v1 op_sel_hi:[0,0,0]
	v_mfma_scale_f32_16x16x128_f8f6f4 v[110:113], v[2:9], v[198:205], v[110:113], v1, v1 op_sel_hi:[0,0,0]
	v_mfma_scale_f32_16x16x128_f8f6f4 v[118:121], v[10:17], v[198:205], v[118:121], v1, v1 op_sel_hi:[0,0,0]
	v_mfma_scale_f32_16x16x128_f8f6f4 v[134:137], v[10:17], v[190:197], v[134:137], v1, v1 op_sel_hi:[0,0,0]
	v_mfma_scale_f32_16x16x128_f8f6f4 v[126:129], v[2:9], v[190:197], v[126:129], v1, v1 op_sel_hi:[0,0,0]
	v_mfma_scale_f32_16x16x128_f8f6f4 v[142:145], v[2:9], v[174:181], v[142:145], v1, v1 op_sel_hi:[0,0,0]
	v_mfma_scale_f32_16x16x128_f8f6f4 v[150:153], v[10:17], v[174:181], v[150:153], v1, v1 op_sel_hi:[0,0,0]
	s_setprio 0
	s_barrier
	s_mov_b32 m0, s38
	v_lshl_add_u64 v[174:175], s[20:21], 0, v[164:165]
	s_add_u32 s48, s20, 0x80000
	ds_read_b128 v[190:193], v186 offset:16384
	ds_read_b128 v[194:197], v186 offset:17408
	ds_read_b128 v[198:201], v186 offset:18432
	ds_read_b128 v[202:205], v186 offset:19456
	ds_read_b128 v[206:209], v186 offset:20480
	ds_read_b128 v[210:213], v186 offset:21504
	ds_read_b128 v[214:217], v186 offset:22528
	ds_read_b128 v[218:221], v186 offset:23552
	global_load_lds_dwordx4 v[174:175], off
	v_lshl_add_u64 v[176:177], s[20:21], 0, v[168:169]
	s_mov_b32 m0, s39
	s_addc_u32 s49, s21, 0
	global_load_lds_dwordx4 v[176:177], off
	v_lshl_add_u64 v[178:179], s[48:49], 0, v[164:165]
	s_mov_b32 m0, s40
	v_lshl_add_u64 v[180:181], s[22:23], 0, v[166:167]
	global_load_lds_dwordx4 v[178:179], off
	v_lshl_add_u64 v[178:179], s[48:49], 0, v[168:169]
	s_mov_b32 m0, s41
	s_nop 0
	global_load_lds_dwordx4 v[178:179], off
	v_lshl_add_u64 v[178:179], s[22:23], 0, v[162:163]
	s_mov_b32 m0, s24
	s_nop 0
	global_load_lds_dwordx4 v[178:179], off
	s_mov_b32 m0, s25
	s_nop 0
	global_load_lds_dwordx4 v[180:181], off
	s_waitcnt vmcnt(8)
	s_waitcnt lgkmcnt(0)
	s_barrier
	s_setprio 1
	s_waitcnt lgkmcnt(0)
	v_mfma_scale_f32_16x16x128_f8f6f4 v[94:97], v[26:33], v[190:197], v[94:97], v1, v1 op_sel_hi:[0,0,0]
	v_mfma_scale_f32_16x16x128_f8f6f4 v[90:93], v[18:25], v[190:197], v[90:93], v1, v1 op_sel_hi:[0,0,0]
	v_mfma_scale_f32_16x16x128_f8f6f4 v[74:77], v[18:25], v[198:205], v[74:77], v1, v1 op_sel_hi:[0,0,0]
	v_mfma_scale_f32_16x16x128_f8f6f4 v[82:85], v[26:33], v[198:205], v[82:85], v1, v1 op_sel_hi:[0,0,0]
	v_mfma_scale_f32_16x16x128_f8f6f4 v[66:69], v[26:33], v[206:213], v[66:69], v1, v1 op_sel_hi:[0,0,0]
	v_mfma_scale_f32_16x16x128_f8f6f4 v[58:61], v[18:25], v[206:213], v[58:61], v1, v1 op_sel_hi:[0,0,0]
	v_mfma_scale_f32_16x16x128_f8f6f4 v[42:45], v[18:25], v[214:221], v[42:45], v1, v1 op_sel_hi:[0,0,0]
	v_mfma_scale_f32_16x16x128_f8f6f4 v[50:53], v[26:33], v[214:221], v[50:53], v1, v1 op_sel_hi:[0,0,0]
	s_setprio 0
	s_setprio 1
	v_mfma_scale_f32_16x16x128_f8f6f4 v[38:41], v[10:17], v[214:221], v[38:41], v1, v1 op_sel_hi:[0,0,0]
	v_mfma_scale_f32_16x16x128_f8f6f4 v[34:37], v[2:9], v[214:221], v[34:37], v1, v1 op_sel_hi:[0,0,0]
	v_mfma_scale_f32_16x16x128_f8f6f4 v[46:49], v[2:9], v[206:213], v[46:49], v1, v1 op_sel_hi:[0,0,0]
	v_mfma_scale_f32_16x16x128_f8f6f4 v[54:57], v[10:17], v[206:213], v[54:57], v1, v1 op_sel_hi:[0,0,0]
	v_mfma_scale_f32_16x16x128_f8f6f4 v[70:73], v[10:17], v[198:205], v[70:73], v1, v1 op_sel_hi:[0,0,0]
	v_mfma_scale_f32_16x16x128_f8f6f4 v[62:65], v[2:9], v[198:205], v[62:65], v1, v1 op_sel_hi:[0,0,0]
	v_mfma_scale_f32_16x16x128_f8f6f4 v[78:81], v[2:9], v[190:197], v[78:81], v1, v1 op_sel_hi:[0,0,0]
	v_mfma_scale_f32_16x16x128_f8f6f4 v[86:89], v[10:17], v[190:197], v[86:89], v1, v1 op_sel_hi:[0,0,0]
	s_setprio 0
	s_barrier
	ds_read_b128 v[2:5], v187
	ds_read_b128 v[6:9], v187 offset:1024
	ds_read_b128 v[10:13], v187 offset:2048
	ds_read_b128 v[14:17], v187 offset:3072
	ds_read_b128 v[18:21], v188
	ds_read_b128 v[22:25], v188 offset:1024
	ds_read_b128 v[26:29], v188 offset:2048
	ds_read_b128 v[30:33], v188 offset:3072
	s_add_u32 s22, s22, 0x80000
	s_addc_u32 s23, s23, 0
	s_mov_b32 m0, s26
	v_lshl_add_u64 v[222:223], s[22:23], 0, v[162:163]
	ds_read_b128 v[190:193], v186 offset:32768
	ds_read_b128 v[194:197], v186 offset:33792
	ds_read_b128 v[198:201], v186 offset:34816
	ds_read_b128 v[202:205], v186 offset:35840
	ds_read_b128 v[206:209], v186 offset:36864
	ds_read_b128 v[210:213], v186 offset:37888
	ds_read_b128 v[214:217], v186 offset:38912
	ds_read_b128 v[218:221], v186 offset:39936
	global_load_lds_dwordx4 v[222:223], off
	v_lshl_add_u64 v[222:223], s[22:23], 0, v[166:167]
	s_mov_b32 m0, s27
	s_nop 0
	global_load_lds_dwordx4 v[222:223], off
	s_waitcnt vmcnt(8)
	s_waitcnt lgkmcnt(0)
	s_barrier
	s_setprio 1
	s_waitcnt lgkmcnt(0)
	v_mfma_scale_f32_16x16x128_f8f6f4 v[158:161], v[2:9], v[190:197], v[158:161], v1, v1 op_sel_hi:[0,0,0]
	v_mfma_scale_f32_16x16x128_f8f6f4 v[154:157], v[10:17], v[190:197], v[154:157], v1, v1 op_sel_hi:[0,0,0]
	v_mfma_scale_f32_16x16x128_f8f6f4 v[138:141], v[10:17], v[198:205], v[138:141], v1, v1 op_sel_hi:[0,0,0]
	v_mfma_scale_f32_16x16x128_f8f6f4 v[146:149], v[2:9], v[198:205], v[146:149], v1, v1 op_sel_hi:[0,0,0]
	v_mfma_scale_f32_16x16x128_f8f6f4 v[130:133], v[2:9], v[206:213], v[130:133], v1, v1 op_sel_hi:[0,0,0]
	v_mfma_scale_f32_16x16x128_f8f6f4 v[122:125], v[10:17], v[206:213], v[122:125], v1, v1 op_sel_hi:[0,0,0]
	v_mfma_scale_f32_16x16x128_f8f6f4 v[106:109], v[10:17], v[214:221], v[106:109], v1, v1 op_sel_hi:[0,0,0]
	v_mfma_scale_f32_16x16x128_f8f6f4 v[114:117], v[2:9], v[214:221], v[114:117], v1, v1 op_sel_hi:[0,0,0]
	s_setprio 0
	s_setprio 1
	v_mfma_scale_f32_16x16x128_f8f6f4 v[102:105], v[18:25], v[214:221], v[102:105], v1, v1 op_sel_hi:[0,0,0]
	v_mfma_scale_f32_16x16x128_f8f6f4 v[98:101], v[26:33], v[214:221], v[98:101], v1, v1 op_sel_hi:[0,0,0]
	v_mfma_scale_f32_16x16x128_f8f6f4 v[110:113], v[26:33], v[206:213], v[110:113], v1, v1 op_sel_hi:[0,0,0]
	v_mfma_scale_f32_16x16x128_f8f6f4 v[118:121], v[18:25], v[206:213], v[118:121], v1, v1 op_sel_hi:[0,0,0]
	v_mfma_scale_f32_16x16x128_f8f6f4 v[134:137], v[18:25], v[198:205], v[134:137], v1, v1 op_sel_hi:[0,0,0]
	v_mfma_scale_f32_16x16x128_f8f6f4 v[126:129], v[26:33], v[198:205], v[126:129], v1, v1 op_sel_hi:[0,0,0]
	v_mfma_scale_f32_16x16x128_f8f6f4 v[142:145], v[26:33], v[190:197], v[142:145], v1, v1 op_sel_hi:[0,0,0]
	v_mfma_scale_f32_16x16x128_f8f6f4 v[150:153], v[18:25], v[190:197], v[150:153], v1, v1 op_sel_hi:[0,0,0]
	s_setprio 0
	s_barrier
	s_mov_b32 m0, s42
	v_lshl_add_u64 v[174:175], v[174:175], 0, s[12:13]
	s_add_u32 s20, s20, 0x80080
	ds_read_b128 v[190:193], v186 offset:49152
	ds_read_b128 v[194:197], v186 offset:50176
	ds_read_b128 v[198:201], v186 offset:51200
	ds_read_b128 v[202:205], v186 offset:52224
	ds_read_b128 v[206:209], v186 offset:53248
	ds_read_b128 v[210:213], v186 offset:54272
	ds_read_b128 v[214:217], v186 offset:55296
	ds_read_b128 v[218:221], v186 offset:56320
	global_load_lds_dwordx4 v[174:175], off
	v_lshl_add_u64 v[174:175], v[176:177], 0, s[12:13]
	s_mov_b32 m0, s43
	s_addc_u32 s21, s21, 0
	global_load_lds_dwordx4 v[174:175], off
	v_lshl_add_u64 v[174:175], s[20:21], 0, v[164:165]
	s_mov_b32 m0, s44
	s_nop 0
	global_load_lds_dwordx4 v[174:175], off
	v_lshl_add_u64 v[174:175], s[20:21], 0, v[168:169]
	s_mov_b32 m0, s45
	s_nop 0
	global_load_lds_dwordx4 v[174:175], off
	v_lshl_add_u64 v[174:175], v[178:179], 0, s[12:13]
	s_mov_b32 m0, s29
	s_nop 0
	global_load_lds_dwordx4 v[174:175], off
	v_lshl_add_u64 v[174:175], v[180:181], 0, s[12:13]
	s_mov_b32 m0, s30
	s_nop 0
	global_load_lds_dwordx4 v[174:175], off
	s_waitcnt vmcnt(8)
	s_waitcnt lgkmcnt(0)
	s_barrier
	s_setprio 1
	s_waitcnt lgkmcnt(0)
	v_mfma_scale_f32_16x16x128_f8f6f4 v[94:97], v[2:9], v[190:197], v[94:97], v1, v1 op_sel_hi:[0,0,0]
	v_mfma_scale_f32_16x16x128_f8f6f4 v[90:93], v[10:17], v[190:197], v[90:93], v1, v1 op_sel_hi:[0,0,0]
	v_mfma_scale_f32_16x16x128_f8f6f4 v[74:77], v[10:17], v[198:205], v[74:77], v1, v1 op_sel_hi:[0,0,0]
	v_mfma_scale_f32_16x16x128_f8f6f4 v[82:85], v[2:9], v[198:205], v[82:85], v1, v1 op_sel_hi:[0,0,0]
	v_mfma_scale_f32_16x16x128_f8f6f4 v[66:69], v[2:9], v[206:213], v[66:69], v1, v1 op_sel_hi:[0,0,0]
	v_mfma_scale_f32_16x16x128_f8f6f4 v[58:61], v[10:17], v[206:213], v[58:61], v1, v1 op_sel_hi:[0,0,0]
	v_mfma_scale_f32_16x16x128_f8f6f4 v[42:45], v[10:17], v[214:221], v[42:45], v1, v1 op_sel_hi:[0,0,0]
	v_mfma_scale_f32_16x16x128_f8f6f4 v[50:53], v[2:9], v[214:221], v[50:53], v1, v1 op_sel_hi:[0,0,0]
	s_setprio 0
	s_setprio 1
	v_mfma_scale_f32_16x16x128_f8f6f4 v[38:41], v[18:25], v[214:221], v[38:41], v1, v1 op_sel_hi:[0,0,0]
	v_mfma_scale_f32_16x16x128_f8f6f4 v[34:37], v[26:33], v[214:221], v[34:37], v1, v1 op_sel_hi:[0,0,0]
	v_mfma_scale_f32_16x16x128_f8f6f4 v[46:49], v[26:33], v[206:213], v[46:49], v1, v1 op_sel_hi:[0,0,0]
	v_mfma_scale_f32_16x16x128_f8f6f4 v[54:57], v[18:25], v[206:213], v[54:57], v1, v1 op_sel_hi:[0,0,0]
	v_mfma_scale_f32_16x16x128_f8f6f4 v[70:73], v[18:25], v[198:205], v[70:73], v1, v1 op_sel_hi:[0,0,0]
	v_mfma_scale_f32_16x16x128_f8f6f4 v[62:65], v[26:33], v[198:205], v[62:65], v1, v1 op_sel_hi:[0,0,0]
	v_mfma_scale_f32_16x16x128_f8f6f4 v[78:81], v[26:33], v[190:197], v[78:81], v1, v1 op_sel_hi:[0,0,0]
	v_mfma_scale_f32_16x16x128_f8f6f4 v[86:89], v[18:25], v[190:197], v[86:89], v1, v1 op_sel_hi:[0,0,0]
	s_setprio 0
	s_barrier
	s_add_i32 s35, s35, 2
	s_add_u32 s16, s16, 0x100
	s_addc_u32 s17, s17, 0
	s_cmp_gt_u32 s35, 13
	s_cbranch_scc0 .LBB0_1291
	s_cmpk_lt_u32 s19, 0x100
	s_cbranch_scc0 .LBB0_1294
	s_barrier

.LBB0_1309:
	ds_read_b128 v[26:29], v189
	ds_read_b128 v[30:33], v189 offset:1024
	ds_read_b128 v[18:21], v189 offset:2048
	ds_read_b128 v[22:25], v189 offset:3072
	ds_read_b128 v[10:13], v190
	ds_read_b128 v[14:17], v190 offset:1024
	ds_read_b128 v[2:5], v190 offset:2048
	ds_read_b128 v[6:9], v190 offset:3072
	s_add_u32 s40, s38, 0xfff80080
	s_addc_u32 s41, s39, -1
	s_cmp_eq_u32 s72, 28
	s_cselect_b32 s43, s18, s41
	s_cselect_b32 s42, s19, s40
	s_cselect_b32 s41, s27, s71
	s_cselect_b32 s40, s29, s70
	v_lshl_add_u64 v[216:217], s[38:39], 0, v[170:171]
	s_add_i32 m0, s37, 0xc000
	ds_read_b128 v[178:181], v191
	ds_read_b128 v[182:185], v191 offset:1024
	ds_read_b128 v[192:195], v191 offset:2048
	ds_read_b128 v[196:199], v191 offset:3072
	ds_read_b128 v[200:203], v191 offset:4096
	ds_read_b128 v[204:207], v191 offset:5120
	ds_read_b128 v[208:211], v191 offset:6144
	ds_read_b128 v[212:215], v191 offset:7168
	global_load_lds_dwordx4 v[216:217], off
	v_lshl_add_u64 v[216:217], s[38:39], 0, v[172:173]
	s_add_i32 m0, s37, 0xe000
	s_nop 0
	global_load_lds_dwordx4 v[216:217], off
	s_waitcnt vmcnt(8)
	s_waitcnt lgkmcnt(0)
	s_barrier
	s_setprio 1
	s_waitcnt lgkmcnt(0)
	v_mfma_scale_f32_16x16x128_f8f6f4 v[158:161], v[26:33], v[178:185], v[158:161], v1, v1 op_sel_hi:[0,0,0]
	v_mfma_scale_f32_16x16x128_f8f6f4 v[154:157], v[18:25], v[178:185], v[154:157], v1, v1 op_sel_hi:[0,0,0]
	v_mfma_scale_f32_16x16x128_f8f6f4 v[138:141], v[18:25], v[192:199], v[138:141], v1, v1 op_sel_hi:[0,0,0]
	v_mfma_scale_f32_16x16x128_f8f6f4 v[146:149], v[26:33], v[192:199], v[146:149], v1, v1 op_sel_hi:[0,0,0]
	v_mfma_scale_f32_16x16x128_f8f6f4 v[130:133], v[26:33], v[200:207], v[130:133], v1, v1 op_sel_hi:[0,0,0]
	v_mfma_scale_f32_16x16x128_f8f6f4 v[122:125], v[18:25], v[200:207], v[122:125], v1, v1 op_sel_hi:[0,0,0]
	v_mfma_scale_f32_16x16x128_f8f6f4 v[106:109], v[18:25], v[208:215], v[106:109], v1, v1 op_sel_hi:[0,0,0]
	v_mfma_scale_f32_16x16x128_f8f6f4 v[114:117], v[26:33], v[208:215], v[114:117], v1, v1 op_sel_hi:[0,0,0]
	s_setprio 0
	s_setprio 1
	v_mfma_scale_f32_16x16x128_f8f6f4 v[102:105], v[10:17], v[208:215], v[102:105], v1, v1 op_sel_hi:[0,0,0]
	v_mfma_scale_f32_16x16x128_f8f6f4 v[98:101], v[2:9], v[208:215], v[98:101], v1, v1 op_sel_hi:[0,0,0]
	v_mfma_scale_f32_16x16x128_f8f6f4 v[110:113], v[2:9], v[200:207], v[110:113], v1, v1 op_sel_hi:[0,0,0]
	v_mfma_scale_f32_16x16x128_f8f6f4 v[118:121], v[10:17], v[200:207], v[118:121], v1, v1 op_sel_hi:[0,0,0]
	v_mfma_scale_f32_16x16x128_f8f6f4 v[134:137], v[10:17], v[192:199], v[134:137], v1, v1 op_sel_hi:[0,0,0]
	v_mfma_scale_f32_16x16x128_f8f6f4 v[126:129], v[2:9], v[192:199], v[126:129], v1, v1 op_sel_hi:[0,0,0]
	v_mfma_scale_f32_16x16x128_f8f6f4 v[142:145], v[2:9], v[178:185], v[142:145], v1, v1 op_sel_hi:[0,0,0]
	v_mfma_scale_f32_16x16x128_f8f6f4 v[150:153], v[10:17], v[178:185], v[150:153], v1, v1 op_sel_hi:[0,0,0]
	s_setprio 0
	s_barrier
	s_add_i32 s64, s59, s3
	v_lshl_add_u64 v[178:179], s[40:41], 0, v[166:167]
	s_mov_b32 m0, s64
	ds_read_b128 v[192:195], v191 offset:16384
	ds_read_b128 v[196:199], v191 offset:17408
	ds_read_b128 v[200:203], v191 offset:18432
	ds_read_b128 v[204:207], v191 offset:19456
	ds_read_b128 v[208:211], v191 offset:20480
	ds_read_b128 v[212:215], v191 offset:21504
	ds_read_b128 v[216:219], v191 offset:22528
	ds_read_b128 v[220:223], v191 offset:23552
	global_load_lds_dwordx4 v[178:179], off
	s_add_i32 m0, s64, 0x2000
	s_add_u32 s64, s40, 0x80000
	v_lshl_add_u64 v[180:181], s[40:41], 0, v[162:163]
	s_addc_u32 s65, s41, 0
	s_add_i32 s73, s62, s3
	global_load_lds_dwordx4 v[180:181], off
	v_lshl_add_u64 v[182:183], s[64:65], 0, v[166:167]
	s_mov_b32 m0, s73
	v_lshl_add_u64 v[184:185], s[42:43], 0, v[164:165]
	global_load_lds_dwordx4 v[182:183], off
	v_lshl_add_u64 v[182:183], s[64:65], 0, v[162:163]
	s_add_i32 m0, s73, 0x2000
	s_nop 0
	global_load_lds_dwordx4 v[182:183], off
	v_lshl_add_u64 v[182:183], s[42:43], 0, v[168:169]
	s_mov_b32 m0, s37
	s_nop 0
	global_load_lds_dwordx4 v[182:183], off
	s_mov_b32 m0, s44
	s_nop 0
	global_load_lds_dwordx4 v[184:185], off
	s_waitcnt vmcnt(8)
	s_waitcnt lgkmcnt(0)
	s_barrier
	s_setprio 1
	s_waitcnt lgkmcnt(0)
	v_mfma_scale_f32_16x16x128_f8f6f4 v[94:97], v[26:33], v[192:199], v[94:97], v1, v1 op_sel_hi:[0,0,0]
	v_mfma_scale_f32_16x16x128_f8f6f4 v[90:93], v[18:25], v[192:199], v[90:93], v1, v1 op_sel_hi:[0,0,0]
	v_mfma_scale_f32_16x16x128_f8f6f4 v[74:77], v[18:25], v[200:207], v[74:77], v1, v1 op_sel_hi:[0,0,0]
	v_mfma_scale_f32_16x16x128_f8f6f4 v[82:85], v[26:33], v[200:207], v[82:85], v1, v1 op_sel_hi:[0,0,0]
	v_mfma_scale_f32_16x16x128_f8f6f4 v[66:69], v[26:33], v[208:215], v[66:69], v1, v1 op_sel_hi:[0,0,0]
	v_mfma_scale_f32_16x16x128_f8f6f4 v[58:61], v[18:25], v[208:215], v[58:61], v1, v1 op_sel_hi:[0,0,0]
	v_mfma_scale_f32_16x16x128_f8f6f4 v[42:45], v[18:25], v[216:223], v[42:45], v1, v1 op_sel_hi:[0,0,0]
	v_mfma_scale_f32_16x16x128_f8f6f4 v[50:53], v[26:33], v[216:223], v[50:53], v1, v1 op_sel_hi:[0,0,0]
	s_setprio 0
	s_setprio 1
	v_mfma_scale_f32_16x16x128_f8f6f4 v[38:41], v[10:17], v[216:223], v[38:41], v1, v1 op_sel_hi:[0,0,0]
	v_mfma_scale_f32_16x16x128_f8f6f4 v[34:37], v[2:9], v[216:223], v[34:37], v1, v1 op_sel_hi:[0,0,0]
	v_mfma_scale_f32_16x16x128_f8f6f4 v[46:49], v[2:9], v[208:215], v[46:49], v1, v1 op_sel_hi:[0,0,0]
	v_mfma_scale_f32_16x16x128_f8f6f4 v[54:57], v[10:17], v[208:215], v[54:57], v1, v1 op_sel_hi:[0,0,0]
	v_mfma_scale_f32_16x16x128_f8f6f4 v[70:73], v[10:17], v[200:207], v[70:73], v1, v1 op_sel_hi:[0,0,0]
	v_mfma_scale_f32_16x16x128_f8f6f4 v[62:65], v[2:9], v[200:207], v[62:65], v1, v1 op_sel_hi:[0,0,0]
	v_mfma_scale_f32_16x16x128_f8f6f4 v[78:81], v[2:9], v[192:199], v[78:81], v1, v1 op_sel_hi:[0,0,0]
	v_mfma_scale_f32_16x16x128_f8f6f4 v[86:89], v[10:17], v[192:199], v[86:89], v1, v1 op_sel_hi:[0,0,0]
	s_setprio 0
	s_barrier
	s_add_i32 s64, 0, 0x18000
	s_add_i32 s65, 0, 0x1c000
	v_add_u32_e32 v14, s64, v187
	v_add_u32_e32 v30, s65, v187
	ds_read_b128 v[2:5], v14
	ds_read_b128 v[6:9], v14 offset:1024
	ds_read_b128 v[10:13], v14 offset:2048
	ds_read_b128 v[14:17], v14 offset:3072
	ds_read_b128 v[18:21], v30
	ds_read_b128 v[22:25], v30 offset:1024
	ds_read_b128 v[26:29], v30 offset:2048
	ds_read_b128 v[30:33], v30 offset:3072
	s_add_u32 s42, s42, 0x80000
	s_addc_u32 s43, s43, 0
	s_mov_b32 m0, s45
	v_lshl_add_u64 v[224:225], s[42:43], 0, v[168:169]
	ds_read_b128 v[192:195], v191 offset:32768
	ds_read_b128 v[196:199], v191 offset:33792
	ds_read_b128 v[200:203], v191 offset:34816
	ds_read_b128 v[204:207], v191 offset:35840
	ds_read_b128 v[208:211], v191 offset:36864
	ds_read_b128 v[212:215], v191 offset:37888
	ds_read_b128 v[216:219], v191 offset:38912
	ds_read_b128 v[220:223], v191 offset:39936
	global_load_lds_dwordx4 v[224:225], off
	v_lshl_add_u64 v[224:225], s[42:43], 0, v[164:165]
	s_mov_b32 m0, s48
	s_nop 0
	global_load_lds_dwordx4 v[224:225], off
	s_waitcnt vmcnt(8)
	s_waitcnt lgkmcnt(0)
	s_barrier
	s_setprio 1
	s_waitcnt lgkmcnt(0)
	v_mfma_scale_f32_16x16x128_f8f6f4 v[158:161], v[2:9], v[192:199], v[158:161], v1, v1 op_sel_hi:[0,0,0]
	v_mfma_scale_f32_16x16x128_f8f6f4 v[154:157], v[10:17], v[192:199], v[154:157], v1, v1 op_sel_hi:[0,0,0]
	v_mfma_scale_f32_16x16x128_f8f6f4 v[138:141], v[10:17], v[200:207], v[138:141], v1, v1 op_sel_hi:[0,0,0]
	v_mfma_scale_f32_16x16x128_f8f6f4 v[146:149], v[2:9], v[200:207], v[146:149], v1, v1 op_sel_hi:[0,0,0]
	v_mfma_scale_f32_16x16x128_f8f6f4 v[130:133], v[2:9], v[208:215], v[130:133], v1, v1 op_sel_hi:[0,0,0]
	v_mfma_scale_f32_16x16x128_f8f6f4 v[122:125], v[10:17], v[208:215], v[122:125], v1, v1 op_sel_hi:[0,0,0]
	v_mfma_scale_f32_16x16x128_f8f6f4 v[106:109], v[10:17], v[216:223], v[106:109], v1, v1 op_sel_hi:[0,0,0]
	v_mfma_scale_f32_16x16x128_f8f6f4 v[114:117], v[2:9], v[216:223], v[114:117], v1, v1 op_sel_hi:[0,0,0]
	s_setprio 0
	s_setprio 1
	v_mfma_scale_f32_16x16x128_f8f6f4 v[102:105], v[18:25], v[216:223], v[102:105], v1, v1 op_sel_hi:[0,0,0]
	v_mfma_scale_f32_16x16x128_f8f6f4 v[98:101], v[26:33], v[216:223], v[98:101], v1, v1 op_sel_hi:[0,0,0]
	v_mfma_scale_f32_16x16x128_f8f6f4 v[110:113], v[26:33], v[208:215], v[110:113], v1, v1 op_sel_hi:[0,0,0]
	v_mfma_scale_f32_16x16x128_f8f6f4 v[118:121], v[18:25], v[208:215], v[118:121], v1, v1 op_sel_hi:[0,0,0]
	v_mfma_scale_f32_16x16x128_f8f6f4 v[134:137], v[18:25], v[200:207], v[134:137], v1, v1 op_sel_hi:[0,0,0]
	v_mfma_scale_f32_16x16x128_f8f6f4 v[126:129], v[26:33], v[200:207], v[126:129], v1, v1 op_sel_hi:[0,0,0]
	v_mfma_scale_f32_16x16x128_f8f6f4 v[142:145], v[26:33], v[192:199], v[142:145], v1, v1 op_sel_hi:[0,0,0]
	v_mfma_scale_f32_16x16x128_f8f6f4 v[150:153], v[18:25], v[192:199], v[150:153], v1, v1 op_sel_hi:[0,0,0]
	s_setprio 0
	s_barrier
	s_add_i32 s42, s64, s3
	v_lshl_add_u64 v[178:179], v[178:179], 0, s[12:13]
	s_mov_b32 m0, s42
	ds_read_b128 v[192:195], v191 offset:49152
	ds_read_b128 v[196:199], v191 offset:50176
	ds_read_b128 v[200:203], v191 offset:51200
	ds_read_b128 v[204:207], v191 offset:52224
	ds_read_b128 v[208:211], v191 offset:53248
	ds_read_b128 v[212:215], v191 offset:54272
	ds_read_b128 v[216:219], v191 offset:55296
	ds_read_b128 v[220:223], v191 offset:56320
	global_load_lds_dwordx4 v[178:179], off
	s_add_i32 m0, s42, 0x2000
	s_add_u32 s40, s40, 0x80080
	v_lshl_add_u64 v[178:179], v[180:181], 0, s[12:13]
	s_addc_u32 s41, s41, 0
	s_add_i32 s42, s65, s3
	global_load_lds_dwordx4 v[178:179], off
	v_lshl_add_u64 v[178:179], s[40:41], 0, v[166:167]
	s_mov_b32 m0, s42
	s_nop 0
	global_load_lds_dwordx4 v[178:179], off
	v_lshl_add_u64 v[178:179], s[40:41], 0, v[162:163]
	s_add_i32 m0, s42, 0x2000
	s_nop 0
	global_load_lds_dwordx4 v[178:179], off
	v_lshl_add_u64 v[178:179], v[182:183], 0, s[12:13]
	s_mov_b32 m0, s51
	s_nop 0
	global_load_lds_dwordx4 v[178:179], off
	v_lshl_add_u64 v[178:179], v[184:185], 0, s[12:13]
	s_mov_b32 m0, s58
	s_nop 0
	global_load_lds_dwordx4 v[178:179], off
	s_waitcnt vmcnt(8)
	s_waitcnt lgkmcnt(0)
	s_barrier
	s_setprio 1
	s_waitcnt lgkmcnt(0)
	v_mfma_scale_f32_16x16x128_f8f6f4 v[94:97], v[2:9], v[192:199], v[94:97], v1, v1 op_sel_hi:[0,0,0]
	v_mfma_scale_f32_16x16x128_f8f6f4 v[90:93], v[10:17], v[192:199], v[90:93], v1, v1 op_sel_hi:[0,0,0]
	v_mfma_scale_f32_16x16x128_f8f6f4 v[74:77], v[10:17], v[200:207], v[74:77], v1, v1 op_sel_hi:[0,0,0]
	v_mfma_scale_f32_16x16x128_f8f6f4 v[82:85], v[2:9], v[200:207], v[82:85], v1, v1 op_sel_hi:[0,0,0]
	v_mfma_scale_f32_16x16x128_f8f6f4 v[66:69], v[2:9], v[208:215], v[66:69], v1, v1 op_sel_hi:[0,0,0]
	v_mfma_scale_f32_16x16x128_f8f6f4 v[58:61], v[10:17], v[208:215], v[58:61], v1, v1 op_sel_hi:[0,0,0]
	v_mfma_scale_f32_16x16x128_f8f6f4 v[42:45], v[10:17], v[216:223], v[42:45], v1, v1 op_sel_hi:[0,0,0]
	v_mfma_scale_f32_16x16x128_f8f6f4 v[50:53], v[2:9], v[216:223], v[50:53], v1, v1 op_sel_hi:[0,0,0]
	s_setprio 0
	s_setprio 1
	v_mfma_scale_f32_16x16x128_f8f6f4 v[38:41], v[18:25], v[216:223], v[38:41], v1, v1 op_sel_hi:[0,0,0]
	v_mfma_scale_f32_16x16x128_f8f6f4 v[34:37], v[26:33], v[216:223], v[34:37], v1, v1 op_sel_hi:[0,0,0]
	v_mfma_scale_f32_16x16x128_f8f6f4 v[46:49], v[26:33], v[208:215], v[46:49], v1, v1 op_sel_hi:[0,0,0]
	v_mfma_scale_f32_16x16x128_f8f6f4 v[54:57], v[18:25], v[208:215], v[54:57], v1, v1 op_sel_hi:[0,0,0]
	v_mfma_scale_f32_16x16x128_f8f6f4 v[70:73], v[18:25], v[200:207], v[70:73], v1, v1 op_sel_hi:[0,0,0]
	v_mfma_scale_f32_16x16x128_f8f6f4 v[62:65], v[26:33], v[200:207], v[62:65], v1, v1 op_sel_hi:[0,0,0]
	v_mfma_scale_f32_16x16x128_f8f6f4 v[78:81], v[26:33], v[192:199], v[78:81], v1, v1 op_sel_hi:[0,0,0]
	v_mfma_scale_f32_16x16x128_f8f6f4 v[86:89], v[18:25], v[192:199], v[86:89], v1, v1 op_sel_hi:[0,0,0]
	s_setprio 0
	s_barrier
	s_add_i32 s72, s72, 2
	s_add_u32 s38, s38, 0x100
	s_addc_u32 s39, s39, 0
	s_add_u32 s70, s70, 0x100
	s_addc_u32 s71, s71, 0
	s_cmp_gt_u32 s72, 29
	s_cbranch_scc0 .LBB0_1309
	s_and_b64 vcc, exec, s[14:15]
	s_cbranch_vccz .LBB0_1312
	s_barrier

.LBB0_1437:
	v_and_b32_e32 v188, 15, v189
	v_and_b32_e32 v2, 48, v189
	v_lshlrev_b32_e32 v3, 2, v189
	s_and_b32 s8, s6, 3
	s_lshl_b32 s9, s7, 13
	v_lshl_or_b32 v2, v188, 6, v2
	v_and_b32_e32 v3, 32, v3
	v_bitop3_b32 v4, v2, s9, v3 bitop3:0xde
	s_lshl_b32 s9, s8, 12
	v_lshl_add_u64 v[180:181], s[20:21], 0, v[154:155]
	v_bitop3_b32 v2, v2, s9, v3 bitop3:0xde
	s_add_i32 s9, s60, s72
	v_lshl_add_u64 v[178:179], s[20:21], 0, v[182:183]
	v_lshl_add_u64 v[72:73], v[180:181], 0, s[36:37]
	s_mov_b32 m0, s9
	s_add_i32 s19, s9, 0x2000
	s_waitcnt vmcnt(2)
	s_barrier
	global_load_lds_dwordx4 v[72:73], off
	v_lshl_add_u64 v[158:159], v[178:179], 0, s[36:37]
	s_mov_b32 m0, s19
	s_add_i32 s18, s67, 0x8000
	global_load_lds_dwordx4 v[158:159], off
	v_lshl_add_u64 v[70:71], v[172:173], 0, s[36:37]
	s_mov_b32 m0, s18
	s_add_i32 s43, s67, 0xa000
	global_load_lds_dwordx4 v[70:71], off
	v_lshl_add_u64 v[160:161], v[170:171], 0, s[36:37]
	s_mov_b32 m0, s43
	s_add_i32 s44, s61, s72
	global_load_lds_dwordx4 v[160:161], off
	v_lshl_add_u64 v[162:163], s[24:25], 0, v[154:155]
	s_mov_b32 m0, s44
	s_add_i32 s45, s44, 0x2000
	global_load_lds_dwordx4 v[162:163], off
	v_lshl_add_u64 v[164:165], s[24:25], 0, v[182:183]
	s_mov_b32 m0, s45
	s_add_i32 s73, 0, 0x10000
	global_load_lds_dwordx4 v[164:165], off
	v_add_u32_e32 v195, s73, v2
	s_add_i32 s75, 0, 0x14000
	s_waitcnt vmcnt(6)
	s_barrier
	v_add_u32_e32 v194, s75, v2
	v_add_u32_e32 v191, 0, v4
	v_add_u32_e32 v193, s60, v2
	v_add_u32_e32 v192, s61, v2
	ds_read_b128 v[54:57], v195
	ds_read_b128 v[58:61], v195 offset:1024
	ds_read_b128 v[196:199], v195 offset:2048
	ds_read_b128 v[200:203], v195 offset:3072
	ds_read_b128 v[10:13], v194
	ds_read_b128 v[14:17], v194 offset:1024
	ds_read_b128 v[2:5], v194 offset:2048
	ds_read_b128 v[6:9], v194 offset:3072
	s_lshl_b32 s66, s7, 6
	v_lshl_add_u64 v[176:177], s[22:23], 0, v[154:155]
	v_lshl_add_u64 v[174:175], s[22:23], 0, v[182:183]
	s_add_u32 s70, s4, 0x10080
	s_addc_u32 s71, s5, 0
	s_add_i32 s74, s67, 0xc000
	v_lshl_add_u64 v[30:31], s[70:71], 0, v[154:155]
	s_mov_b32 m0, s74
	s_add_i32 s69, s67, 0xe000
	ds_read_b128 v[22:25], v191
	ds_read_b128 v[26:29], v191 offset:1024
	ds_read_b128 v[34:37], v191 offset:2048
	ds_read_b128 v[38:41], v191 offset:3072
	ds_read_b128 v[82:85], v191 offset:4096
	ds_read_b128 v[86:89], v191 offset:5120
	ds_read_b128 v[94:97], v191 offset:6144
	ds_read_b128 v[98:101], v191 offset:7168
	global_load_lds_dwordx4 v[30:31], off
	v_lshl_add_u64 v[30:31], s[70:71], 0, v[182:183]
	s_mov_b32 m0, s69
	s_nop 0
	global_load_lds_dwordx4 v[30:31], off
	s_waitcnt vmcnt(8)
	s_waitcnt lgkmcnt(0)
	s_barrier
	s_setprio 1
	v_mov_b64_e32 v[32:33], v[20:21]
	v_mov_b64_e32 v[152:153], v[20:21]
	v_mov_b64_e32 v[92:93], v[20:21]
	v_mov_b64_e32 v[44:45], v[20:21]
	v_mov_b64_e32 v[116:117], v[20:21]
	v_mov_b64_e32 v[64:65], v[20:21]
	v_mov_b64_e32 v[80:81], v[20:21]
	v_mov_b64_e32 v[52:53], v[20:21]
	v_mov_b64_e32 v[30:31], v[18:19]
	v_mov_b64_e32 v[150:151], v[18:19]
	v_mov_b64_e32 v[90:91], v[18:19]
	v_mov_b64_e32 v[42:43], v[18:19]
	v_mov_b64_e32 v[114:115], v[18:19]
	v_mov_b64_e32 v[62:63], v[18:19]
	v_mov_b64_e32 v[78:79], v[18:19]
	v_mov_b64_e32 v[50:51], v[18:19]
	s_waitcnt lgkmcnt(0)
	v_mfma_scale_f32_16x16x128_f8f6f4 v[30:33], v[54:61], v[22:29], v[30:33], v190, v190 op_sel_hi:[0,0,0]
	v_mfma_scale_f32_16x16x128_f8f6f4 v[150:153], v[196:203], v[22:29], v[150:153], v190, v190 op_sel_hi:[0,0,0]
	v_mfma_scale_f32_16x16x128_f8f6f4 v[42:45], v[196:203], v[34:41], v[42:45], v190, v190 op_sel_hi:[0,0,0]
	v_mfma_scale_f32_16x16x128_f8f6f4 v[90:93], v[54:61], v[34:41], v[90:93], v190, v190 op_sel_hi:[0,0,0]
	v_mfma_scale_f32_16x16x128_f8f6f4 v[114:117], v[54:61], v[82:89], v[114:117], v190, v190 op_sel_hi:[0,0,0]
	v_mfma_scale_f32_16x16x128_f8f6f4 v[62:65], v[196:203], v[82:89], v[62:65], v190, v190 op_sel_hi:[0,0,0]
	v_mfma_scale_f32_16x16x128_f8f6f4 v[50:53], v[196:203], v[94:101], v[50:53], v190, v190 op_sel_hi:[0,0,0]
	v_mfma_scale_f32_16x16x128_f8f6f4 v[78:81], v[54:61], v[94:101], v[78:81], v190, v190 op_sel_hi:[0,0,0]
	s_setprio 0
	s_setprio 1
	v_mov_b64_e32 v[144:145], v[20:21]
	v_mov_b64_e32 v[148:149], v[20:21]
	v_mov_b64_e32 v[142:143], v[18:19]
	v_mov_b64_e32 v[146:147], v[18:19]
	v_mfma_scale_f32_16x16x128_f8f6f4 v[142:145], v[10:17], v[22:29], v[142:145], v190, v190 op_sel_hi:[0,0,0]
	v_mfma_scale_f32_16x16x128_f8f6f4 v[146:149], v[2:9], v[22:29], v[146:149], v190, v190 op_sel_hi:[0,0,0]
	v_mov_b64_e32 v[28:29], v[20:21]
	v_mov_b64_e32 v[140:141], v[20:21]
	v_mov_b64_e32 v[26:27], v[18:19]
	v_mov_b64_e32 v[138:139], v[18:19]
	v_mfma_scale_f32_16x16x128_f8f6f4 v[26:29], v[10:17], v[34:41], v[26:29], v190, v190 op_sel_hi:[0,0,0]
	v_mfma_scale_f32_16x16x128_f8f6f4 v[138:141], v[2:9], v[34:41], v[138:141], v190, v190 op_sel_hi:[0,0,0]
	v_mov_b64_e32 v[40:41], v[20:21]
	v_mov_b64_e32 v[128:129], v[20:21]
	v_mov_b64_e32 v[24:25], v[20:21]
	v_mov_b64_e32 v[76:77], v[20:21]
	v_mov_b64_e32 v[38:39], v[18:19]
	v_mov_b64_e32 v[126:127], v[18:19]
	v_mov_b64_e32 v[22:23], v[18:19]
	v_mov_b64_e32 v[74:75], v[18:19]
	v_mfma_scale_f32_16x16x128_f8f6f4 v[38:41], v[10:17], v[82:89], v[38:41], v190, v190 op_sel_hi:[0,0,0]
	v_mfma_scale_f32_16x16x128_f8f6f4 v[126:129], v[2:9], v[82:89], v[126:129], v190, v190 op_sel_hi:[0,0,0]
	v_mfma_scale_f32_16x16x128_f8f6f4 v[22:25], v[10:17], v[94:101], v[22:25], v190, v190 op_sel_hi:[0,0,0]
	v_mfma_scale_f32_16x16x128_f8f6f4 v[74:77], v[2:9], v[94:101], v[74:77], v190, v190 op_sel_hi:[0,0,0]
	s_setprio 0
	s_barrier
	s_add_i32 s70, s73, s72
	v_lshl_add_u64 v[34:35], v[180:181], 0, s[14:15]
	s_mov_b32 m0, s70
	s_add_i32 s71, s70, 0x2000
	ds_read_b128 v[204:207], v191 offset:16384
	ds_read_b128 v[208:211], v191 offset:17408
	ds_read_b128 v[212:215], v191 offset:18432
	ds_read_b128 v[216:219], v191 offset:19456
	ds_read_b128 v[220:223], v191 offset:20480
	ds_read_b128 v[224:227], v191 offset:21504
	ds_read_b128 v[228:231], v191 offset:22528
	ds_read_b128 v[232:235], v191 offset:23552
	global_load_lds_dwordx4 v[34:35], off
	v_lshl_add_u64 v[34:35], v[178:179], 0, s[14:15]
	s_mov_b32 m0, s71
	s_add_i32 s72, s75, s72
	global_load_lds_dwordx4 v[34:35], off
	v_lshl_add_u64 v[34:35], s[26:27], 0, v[154:155]
	s_mov_b32 m0, s72
	s_add_i32 s73, s72, 0x2000
	global_load_lds_dwordx4 v[34:35], off
	v_lshl_add_u64 v[34:35], s[26:27], 0, v[182:183]
	s_mov_b32 m0, s73
	s_nop 0
	global_load_lds_dwordx4 v[34:35], off
	v_lshl_add_u64 v[34:35], v[172:173], 0, s[14:15]
	s_mov_b32 m0, s67
	s_nop 0
	global_load_lds_dwordx4 v[34:35], off
	v_lshl_add_u64 v[34:35], v[170:171], 0, s[14:15]
	s_mov_b32 m0, s68
	s_nop 0
	global_load_lds_dwordx4 v[34:35], off
	s_waitcnt vmcnt(8)
	s_waitcnt lgkmcnt(0)
	s_barrier
	s_setprio 1
	v_mov_b64_e32 v[136:137], v[20:21]
	v_mov_b64_e32 v[104:105], v[20:21]
	v_mov_b64_e32 v[124:125], v[20:21]
	v_mov_b64_e32 v[100:101], v[20:21]
	v_mov_b64_e32 v[112:113], v[20:21]
	v_mov_b64_e32 v[108:109], v[20:21]
	v_mov_b64_e32 v[88:89], v[20:21]
	v_mov_b64_e32 v[84:85], v[20:21]
	v_mov_b64_e32 v[134:135], v[18:19]
	v_mov_b64_e32 v[102:103], v[18:19]
	v_mov_b64_e32 v[122:123], v[18:19]
	v_mov_b64_e32 v[98:99], v[18:19]
	v_mov_b64_e32 v[110:111], v[18:19]
	v_mov_b64_e32 v[106:107], v[18:19]
	v_mov_b64_e32 v[86:87], v[18:19]
	v_mov_b64_e32 v[82:83], v[18:19]
	s_waitcnt lgkmcnt(0)
	v_mfma_scale_f32_16x16x128_f8f6f4 v[134:137], v[54:61], v[204:211], v[134:137], v190, v190 op_sel_hi:[0,0,0]
	v_mfma_scale_f32_16x16x128_f8f6f4 v[102:105], v[196:203], v[204:211], v[102:105], v190, v190 op_sel_hi:[0,0,0]
	v_mfma_scale_f32_16x16x128_f8f6f4 v[98:101], v[196:203], v[212:219], v[98:101], v190, v190 op_sel_hi:[0,0,0]
	v_mfma_scale_f32_16x16x128_f8f6f4 v[122:125], v[54:61], v[212:219], v[122:125], v190, v190 op_sel_hi:[0,0,0]
	v_mfma_scale_f32_16x16x128_f8f6f4 v[110:113], v[54:61], v[220:227], v[110:113], v190, v190 op_sel_hi:[0,0,0]
	v_mfma_scale_f32_16x16x128_f8f6f4 v[106:109], v[196:203], v[220:227], v[106:109], v190, v190 op_sel_hi:[0,0,0]
	v_mfma_scale_f32_16x16x128_f8f6f4 v[82:85], v[196:203], v[228:235], v[82:85], v190, v190 op_sel_hi:[0,0,0]
	v_mfma_scale_f32_16x16x128_f8f6f4 v[86:89], v[54:61], v[228:235], v[86:89], v190, v190 op_sel_hi:[0,0,0]
	s_setprio 0
	s_setprio 1
	v_mov_b64_e32 v[36:37], v[20:21]
	v_mov_b64_e32 v[132:133], v[20:21]
	v_mov_b64_e32 v[48:49], v[20:21]
	v_mov_b64_e32 v[120:121], v[20:21]
	v_mov_b64_e32 v[68:69], v[20:21]
	v_mov_b64_e32 v[96:97], v[20:21]
	v_mov_b64_e32 v[56:57], v[20:21]
	v_mov_b64_e32 v[60:61], v[20:21]
	v_mov_b64_e32 v[34:35], v[18:19]
	v_mov_b64_e32 v[130:131], v[18:19]
	v_mov_b64_e32 v[46:47], v[18:19]
	v_mov_b64_e32 v[118:119], v[18:19]
	v_mov_b64_e32 v[66:67], v[18:19]
	v_mov_b64_e32 v[94:95], v[18:19]
	v_mov_b64_e32 v[54:55], v[18:19]
	v_mov_b64_e32 v[58:59], v[18:19]
	v_mfma_scale_f32_16x16x128_f8f6f4 v[34:37], v[10:17], v[204:211], v[34:37], v190, v190 op_sel_hi:[0,0,0]
	v_mfma_scale_f32_16x16x128_f8f6f4 v[130:133], v[2:9], v[204:211], v[130:133], v190, v190 op_sel_hi:[0,0,0]
	v_mfma_scale_f32_16x16x128_f8f6f4 v[118:121], v[2:9], v[212:219], v[118:121], v190, v190 op_sel_hi:[0,0,0]
	v_mfma_scale_f32_16x16x128_f8f6f4 v[46:49], v[10:17], v[212:219], v[46:49], v190, v190 op_sel_hi:[0,0,0]
	v_mfma_scale_f32_16x16x128_f8f6f4 v[66:69], v[10:17], v[220:227], v[66:69], v190, v190 op_sel_hi:[0,0,0]
	v_mfma_scale_f32_16x16x128_f8f6f4 v[94:97], v[2:9], v[220:227], v[94:97], v190, v190 op_sel_hi:[0,0,0]
	v_mfma_scale_f32_16x16x128_f8f6f4 v[58:61], v[2:9], v[228:235], v[58:61], v190, v190 op_sel_hi:[0,0,0]
	v_mfma_scale_f32_16x16x128_f8f6f4 v[54:57], v[10:17], v[228:235], v[54:57], v190, v190 op_sel_hi:[0,0,0]
	s_setprio 0
	s_barrier
	ds_read_b128 v[2:5], v193
	ds_read_b128 v[6:9], v193 offset:1024
	ds_read_b128 v[10:13], v193 offset:2048
	ds_read_b128 v[14:17], v193 offset:3072
	ds_read_b128 v[196:199], v192
	ds_read_b128 v[200:203], v192 offset:1024
	ds_read_b128 v[204:207], v192 offset:2048
	ds_read_b128 v[208:211], v192 offset:3072
	s_add_u32 s76, s4, 0x10100
	s_addc_u32 s77, s5, 0
	s_mov_b32 m0, s48
	v_lshl_add_u64 v[244:245], s[76:77], 0, v[154:155]
	ds_read_b128 v[212:215], v191 offset:32768
	ds_read_b128 v[216:219], v191 offset:33792
	ds_read_b128 v[220:223], v191 offset:34816
	ds_read_b128 v[224:227], v191 offset:35840
	ds_read_b128 v[228:231], v191 offset:36864
	ds_read_b128 v[232:235], v191 offset:37888
	ds_read_b128 v[236:239], v191 offset:38912
	ds_read_b128 v[240:243], v191 offset:39936
	global_load_lds_dwordx4 v[244:245], off
	v_lshl_add_u64 v[244:245], s[76:77], 0, v[182:183]
	s_mov_b32 m0, s49
	s_nop 0
	global_load_lds_dwordx4 v[244:245], off
	s_waitcnt vmcnt(8)
	s_waitcnt lgkmcnt(0)
	s_barrier
	s_setprio 1
	s_waitcnt lgkmcnt(0)
	v_mfma_scale_f32_16x16x128_f8f6f4 v[30:33], v[2:9], v[212:219], v[30:33], v190, v190 op_sel_hi:[0,0,0]
	v_mfma_scale_f32_16x16x128_f8f6f4 v[150:153], v[10:17], v[212:219], v[150:153], v190, v190 op_sel_hi:[0,0,0]
	v_mfma_scale_f32_16x16x128_f8f6f4 v[42:45], v[10:17], v[220:227], v[42:45], v190, v190 op_sel_hi:[0,0,0]
	v_mfma_scale_f32_16x16x128_f8f6f4 v[90:93], v[2:9], v[220:227], v[90:93], v190, v190 op_sel_hi:[0,0,0]
	v_mfma_scale_f32_16x16x128_f8f6f4 v[114:117], v[2:9], v[228:235], v[114:117], v190, v190 op_sel_hi:[0,0,0]
	v_mfma_scale_f32_16x16x128_f8f6f4 v[62:65], v[10:17], v[228:235], v[62:65], v190, v190 op_sel_hi:[0,0,0]
	v_mfma_scale_f32_16x16x128_f8f6f4 v[50:53], v[10:17], v[236:243], v[50:53], v190, v190 op_sel_hi:[0,0,0]
	v_mfma_scale_f32_16x16x128_f8f6f4 v[78:81], v[2:9], v[236:243], v[78:81], v190, v190 op_sel_hi:[0,0,0]
	s_setprio 0
	s_setprio 1
	v_mfma_scale_f32_16x16x128_f8f6f4 v[22:25], v[196:203], v[236:243], v[22:25], v190, v190 op_sel_hi:[0,0,0]
	v_mfma_scale_f32_16x16x128_f8f6f4 v[74:77], v[204:211], v[236:243], v[74:77], v190, v190 op_sel_hi:[0,0,0]
	v_mfma_scale_f32_16x16x128_f8f6f4 v[126:129], v[204:211], v[228:235], v[126:129], v190, v190 op_sel_hi:[0,0,0]
	v_mfma_scale_f32_16x16x128_f8f6f4 v[38:41], v[196:203], v[228:235], v[38:41], v190, v190 op_sel_hi:[0,0,0]
	v_mfma_scale_f32_16x16x128_f8f6f4 v[26:29], v[196:203], v[220:227], v[26:29], v190, v190 op_sel_hi:[0,0,0]
	v_mfma_scale_f32_16x16x128_f8f6f4 v[138:141], v[204:211], v[220:227], v[138:141], v190, v190 op_sel_hi:[0,0,0]
	v_mfma_scale_f32_16x16x128_f8f6f4 v[146:149], v[204:211], v[212:219], v[146:149], v190, v190 op_sel_hi:[0,0,0]
	v_mfma_scale_f32_16x16x128_f8f6f4 v[142:145], v[196:203], v[212:219], v[142:145], v190, v190 op_sel_hi:[0,0,0]
	s_setprio 0
	s_barrier
	s_mov_b32 m0, s9
	v_lshl_add_u64 v[244:245], v[180:181], 0, s[38:39]
	ds_read_b128 v[212:215], v191 offset:49152
	ds_read_b128 v[216:219], v191 offset:50176
	ds_read_b128 v[220:223], v191 offset:51200
	ds_read_b128 v[224:227], v191 offset:52224
	ds_read_b128 v[228:231], v191 offset:53248
	ds_read_b128 v[232:235], v191 offset:54272
	ds_read_b128 v[236:239], v191 offset:55296
	ds_read_b128 v[240:243], v191 offset:56320
	global_load_lds_dwordx4 v[244:245], off
	v_lshl_add_u64 v[244:245], v[178:179], 0, s[38:39]
	s_mov_b32 m0, s19
	s_nop 0
	global_load_lds_dwordx4 v[244:245], off
	v_lshl_add_u64 v[244:245], s[28:29], 0, v[154:155]
	s_mov_b32 m0, s44
	s_nop 0
	global_load_lds_dwordx4 v[244:245], off
	v_lshl_add_u64 v[244:245], s[28:29], 0, v[182:183]
	s_mov_b32 m0, s45
	s_nop 0
	global_load_lds_dwordx4 v[244:245], off
	v_lshl_add_u64 v[244:245], v[172:173], 0, s[38:39]
	s_mov_b32 m0, s18
	s_nop 0
	global_load_lds_dwordx4 v[244:245], off
	v_lshl_add_u64 v[244:245], v[170:171], 0, s[38:39]
	s_mov_b32 m0, s43
	s_nop 0
	global_load_lds_dwordx4 v[244:245], off
	s_waitcnt vmcnt(8)
	s_waitcnt lgkmcnt(0)
	s_barrier
	s_setprio 1
	s_waitcnt lgkmcnt(0)
	v_mfma_scale_f32_16x16x128_f8f6f4 v[134:137], v[2:9], v[212:219], v[134:137], v190, v190 op_sel_hi:[0,0,0]
	v_mfma_scale_f32_16x16x128_f8f6f4 v[102:105], v[10:17], v[212:219], v[102:105], v190, v190 op_sel_hi:[0,0,0]
	v_mfma_scale_f32_16x16x128_f8f6f4 v[98:101], v[10:17], v[220:227], v[98:101], v190, v190 op_sel_hi:[0,0,0]
	v_mfma_scale_f32_16x16x128_f8f6f4 v[122:125], v[2:9], v[220:227], v[122:125], v190, v190 op_sel_hi:[0,0,0]
	v_mfma_scale_f32_16x16x128_f8f6f4 v[110:113], v[2:9], v[228:235], v[110:113], v190, v190 op_sel_hi:[0,0,0]
	v_mfma_scale_f32_16x16x128_f8f6f4 v[106:109], v[10:17], v[228:235], v[106:109], v190, v190 op_sel_hi:[0,0,0]
	v_mfma_scale_f32_16x16x128_f8f6f4 v[82:85], v[10:17], v[236:243], v[82:85], v190, v190 op_sel_hi:[0,0,0]
	v_mfma_scale_f32_16x16x128_f8f6f4 v[86:89], v[2:9], v[236:243], v[86:89], v190, v190 op_sel_hi:[0,0,0]
	s_setprio 0
	s_setprio 1
	v_mfma_scale_f32_16x16x128_f8f6f4 v[54:57], v[196:203], v[236:243], v[54:57], v190, v190 op_sel_hi:[0,0,0]
	v_mfma_scale_f32_16x16x128_f8f6f4 v[58:61], v[204:211], v[236:243], v[58:61], v190, v190 op_sel_hi:[0,0,0]
	v_mfma_scale_f32_16x16x128_f8f6f4 v[94:97], v[204:211], v[228:235], v[94:97], v190, v190 op_sel_hi:[0,0,0]
	v_mfma_scale_f32_16x16x128_f8f6f4 v[66:69], v[196:203], v[228:235], v[66:69], v190, v190 op_sel_hi:[0,0,0]
	v_mfma_scale_f32_16x16x128_f8f6f4 v[46:49], v[196:203], v[220:227], v[46:49], v190, v190 op_sel_hi:[0,0,0]
	v_mfma_scale_f32_16x16x128_f8f6f4 v[118:121], v[204:211], v[220:227], v[118:121], v190, v190 op_sel_hi:[0,0,0]
	v_mfma_scale_f32_16x16x128_f8f6f4 v[130:133], v[204:211], v[212:219], v[130:133], v190, v190 op_sel_hi:[0,0,0]
	v_mfma_scale_f32_16x16x128_f8f6f4 v[34:37], v[196:203], v[212:219], v[34:37], v190, v190 op_sel_hi:[0,0,0]
	s_setprio 0
	s_barrier
	ds_read_b128 v[2:5], v195
	ds_read_b128 v[6:9], v195 offset:1024
	ds_read_b128 v[10:13], v195 offset:2048
	ds_read_b128 v[14:17], v195 offset:3072
	ds_read_b128 v[196:199], v194
	ds_read_b128 v[200:203], v194 offset:1024
	ds_read_b128 v[204:207], v194 offset:2048
	ds_read_b128 v[208:211], v194 offset:3072
	s_add_u32 s4, s4, 0x10180
	s_addc_u32 s5, s5, 0
	s_mov_b32 m0, s74
	v_lshl_add_u64 v[194:195], s[4:5], 0, v[154:155]
	ds_read_b128 v[212:215], v191
	ds_read_b128 v[216:219], v191 offset:1024
	ds_read_b128 v[220:223], v191 offset:2048
	ds_read_b128 v[224:227], v191 offset:3072
	ds_read_b128 v[228:231], v191 offset:4096
	ds_read_b128 v[232:235], v191 offset:5120
	ds_read_b128 v[236:239], v191 offset:6144
	ds_read_b128 v[240:243], v191 offset:7168
	global_load_lds_dwordx4 v[194:195], off
	v_lshl_add_u64 v[182:183], s[4:5], 0, v[182:183]
	s_mov_b32 m0, s69
	s_nop 0
	global_load_lds_dwordx4 v[182:183], off
	s_waitcnt vmcnt(8)
	s_waitcnt lgkmcnt(0)
	s_barrier
	s_setprio 1
	s_waitcnt lgkmcnt(0)
	v_mfma_scale_f32_16x16x128_f8f6f4 v[30:33], v[2:9], v[212:219], v[30:33], v190, v190 op_sel_hi:[0,0,0]
	v_mfma_scale_f32_16x16x128_f8f6f4 v[150:153], v[10:17], v[212:219], v[150:153], v190, v190 op_sel_hi:[0,0,0]
	v_mfma_scale_f32_16x16x128_f8f6f4 v[42:45], v[10:17], v[220:227], v[42:45], v190, v190 op_sel_hi:[0,0,0]
	v_mfma_scale_f32_16x16x128_f8f6f4 v[90:93], v[2:9], v[220:227], v[90:93], v190, v190 op_sel_hi:[0,0,0]
	v_mfma_scale_f32_16x16x128_f8f6f4 v[114:117], v[2:9], v[228:235], v[114:117], v190, v190 op_sel_hi:[0,0,0]
	v_mfma_scale_f32_16x16x128_f8f6f4 v[62:65], v[10:17], v[228:235], v[62:65], v190, v190 op_sel_hi:[0,0,0]
	v_mfma_scale_f32_16x16x128_f8f6f4 v[50:53], v[10:17], v[236:243], v[50:53], v190, v190 op_sel_hi:[0,0,0]
	v_mfma_scale_f32_16x16x128_f8f6f4 v[78:81], v[2:9], v[236:243], v[78:81], v190, v190 op_sel_hi:[0,0,0]
	s_setprio 0
	s_setprio 1
	v_mfma_scale_f32_16x16x128_f8f6f4 v[22:25], v[196:203], v[236:243], v[22:25], v190, v190 op_sel_hi:[0,0,0]
	v_mfma_scale_f32_16x16x128_f8f6f4 v[74:77], v[204:211], v[236:243], v[74:77], v190, v190 op_sel_hi:[0,0,0]
	v_mfma_scale_f32_16x16x128_f8f6f4 v[126:129], v[204:211], v[228:235], v[126:129], v190, v190 op_sel_hi:[0,0,0]
	v_mfma_scale_f32_16x16x128_f8f6f4 v[38:41], v[196:203], v[228:235], v[38:41], v190, v190 op_sel_hi:[0,0,0]
	v_mfma_scale_f32_16x16x128_f8f6f4 v[26:29], v[196:203], v[220:227], v[26:29], v190, v190 op_sel_hi:[0,0,0]
	v_mfma_scale_f32_16x16x128_f8f6f4 v[138:141], v[204:211], v[220:227], v[138:141], v190, v190 op_sel_hi:[0,0,0]
	v_mfma_scale_f32_16x16x128_f8f6f4 v[146:149], v[204:211], v[212:219], v[146:149], v190, v190 op_sel_hi:[0,0,0]
	v_mfma_scale_f32_16x16x128_f8f6f4 v[142:145], v[196:203], v[212:219], v[142:145], v190, v190 op_sel_hi:[0,0,0]
	s_setprio 0
	s_barrier
	s_mov_b32 m0, s70
	ds_read_b128 v[212:215], v191 offset:16384
	ds_read_b128 v[216:219], v191 offset:17408
	ds_read_b128 v[220:223], v191 offset:18432
	ds_read_b128 v[224:227], v191 offset:19456
	ds_read_b128 v[228:231], v191 offset:20480
	ds_read_b128 v[232:235], v191 offset:21504
	ds_read_b128 v[236:239], v191 offset:22528
	ds_read_b128 v[240:243], v191 offset:23552
	global_load_lds_dwordx4 v[180:181], off
	s_mov_b32 m0, s71
	s_nop 0
	global_load_lds_dwordx4 v[178:179], off
	s_mov_b32 m0, s72
	s_nop 0
	global_load_lds_dwordx4 v[176:177], off
	s_mov_b32 m0, s73
	s_nop 0
	global_load_lds_dwordx4 v[174:175], off
	s_mov_b32 m0, s67
	s_nop 0
	global_load_lds_dwordx4 v[172:173], off
	s_mov_b32 m0, s68
	s_nop 0
	global_load_lds_dwordx4 v[170:171], off
	s_waitcnt vmcnt(8)
	s_waitcnt lgkmcnt(0)
	s_barrier
	s_setprio 1
	s_waitcnt lgkmcnt(0)
	v_mfma_scale_f32_16x16x128_f8f6f4 v[134:137], v[2:9], v[212:219], v[134:137], v190, v190 op_sel_hi:[0,0,0]
	v_mfma_scale_f32_16x16x128_f8f6f4 v[102:105], v[10:17], v[212:219], v[102:105], v190, v190 op_sel_hi:[0,0,0]
	v_mfma_scale_f32_16x16x128_f8f6f4 v[98:101], v[10:17], v[220:227], v[98:101], v190, v190 op_sel_hi:[0,0,0]
	v_mfma_scale_f32_16x16x128_f8f6f4 v[122:125], v[2:9], v[220:227], v[122:125], v190, v190 op_sel_hi:[0,0,0]
	v_mfma_scale_f32_16x16x128_f8f6f4 v[110:113], v[2:9], v[228:235], v[110:113], v190, v190 op_sel_hi:[0,0,0]
	v_mfma_scale_f32_16x16x128_f8f6f4 v[106:109], v[10:17], v[228:235], v[106:109], v190, v190 op_sel_hi:[0,0,0]
	v_mfma_scale_f32_16x16x128_f8f6f4 v[82:85], v[10:17], v[236:243], v[82:85], v190, v190 op_sel_hi:[0,0,0]
	v_mfma_scale_f32_16x16x128_f8f6f4 v[86:89], v[2:9], v[236:243], v[86:89], v190, v190 op_sel_hi:[0,0,0]
	s_setprio 0
	s_setprio 1
	v_mfma_scale_f32_16x16x128_f8f6f4 v[54:57], v[196:203], v[236:243], v[54:57], v190, v190 op_sel_hi:[0,0,0]
	v_mfma_scale_f32_16x16x128_f8f6f4 v[58:61], v[204:211], v[236:243], v[58:61], v190, v190 op_sel_hi:[0,0,0]
	v_mfma_scale_f32_16x16x128_f8f6f4 v[94:97], v[204:211], v[228:235], v[94:97], v190, v190 op_sel_hi:[0,0,0]
	v_mfma_scale_f32_16x16x128_f8f6f4 v[66:69], v[196:203], v[228:235], v[66:69], v190, v190 op_sel_hi:[0,0,0]
	v_mfma_scale_f32_16x16x128_f8f6f4 v[46:49], v[196:203], v[220:227], v[46:49], v190, v190 op_sel_hi:[0,0,0]
	v_mfma_scale_f32_16x16x128_f8f6f4 v[118:121], v[204:211], v[220:227], v[118:121], v190, v190 op_sel_hi:[0,0,0]
	v_mfma_scale_f32_16x16x128_f8f6f4 v[130:133], v[204:211], v[212:219], v[130:133], v190, v190 op_sel_hi:[0,0,0]
	v_mfma_scale_f32_16x16x128_f8f6f4 v[34:37], v[196:203], v[212:219], v[34:37], v190, v190 op_sel_hi:[0,0,0]
	s_setprio 0
	s_barrier
	ds_read_b128 v[2:5], v193
	ds_read_b128 v[6:9], v193 offset:1024
	ds_read_b128 v[10:13], v193 offset:2048
	ds_read_b128 v[14:17], v193 offset:3072
	ds_read_b128 v[170:173], v192
	ds_read_b128 v[174:177], v192 offset:1024
	ds_read_b128 v[194:197], v192 offset:2048
	ds_read_b128 v[198:201], v192 offset:3072
	s_mov_b32 m0, s48
	ds_read_b128 v[202:205], v191 offset:32768
	ds_read_b128 v[206:209], v191 offset:33792
	ds_read_b128 v[210:213], v191 offset:34816
	ds_read_b128 v[214:217], v191 offset:35840
	ds_read_b128 v[218:221], v191 offset:36864
	ds_read_b128 v[222:225], v191 offset:37888
	ds_read_b128 v[226:229], v191 offset:38912
	ds_read_b128 v[230:233], v191 offset:39936
	global_load_lds_dwordx4 v[166:167], off
	s_mov_b32 m0, s49
	s_nop 0
	global_load_lds_dwordx4 v[168:169], off
	s_waitcnt vmcnt(8)
	s_waitcnt lgkmcnt(0)
	s_barrier
	s_setprio 1
	s_waitcnt lgkmcnt(0)
	v_mfma_scale_f32_16x16x128_f8f6f4 v[30:33], v[2:9], v[202:209], v[30:33], v190, v190 op_sel_hi:[0,0,0]
	v_mfma_scale_f32_16x16x128_f8f6f4 v[150:153], v[10:17], v[202:209], v[150:153], v190, v190 op_sel_hi:[0,0,0]
	v_mfma_scale_f32_16x16x128_f8f6f4 v[42:45], v[10:17], v[210:217], v[42:45], v190, v190 op_sel_hi:[0,0,0]
	v_mfma_scale_f32_16x16x128_f8f6f4 v[90:93], v[2:9], v[210:217], v[90:93], v190, v190 op_sel_hi:[0,0,0]
	v_mfma_scale_f32_16x16x128_f8f6f4 v[114:117], v[2:9], v[218:225], v[114:117], v190, v190 op_sel_hi:[0,0,0]
	v_mfma_scale_f32_16x16x128_f8f6f4 v[62:65], v[10:17], v[218:225], v[62:65], v190, v190 op_sel_hi:[0,0,0]
	v_mfma_scale_f32_16x16x128_f8f6f4 v[50:53], v[10:17], v[226:233], v[50:53], v190, v190 op_sel_hi:[0,0,0]
	v_mfma_scale_f32_16x16x128_f8f6f4 v[78:81], v[2:9], v[226:233], v[78:81], v190, v190 op_sel_hi:[0,0,0]
	s_setprio 0
	s_setprio 1
	v_mfma_scale_f32_16x16x128_f8f6f4 v[22:25], v[170:177], v[226:233], v[22:25], v190, v190 op_sel_hi:[0,0,0]
	v_mfma_scale_f32_16x16x128_f8f6f4 v[74:77], v[194:201], v[226:233], v[74:77], v190, v190 op_sel_hi:[0,0,0]
	v_mfma_scale_f32_16x16x128_f8f6f4 v[126:129], v[194:201], v[218:225], v[126:129], v190, v190 op_sel_hi:[0,0,0]
	v_mfma_scale_f32_16x16x128_f8f6f4 v[38:41], v[170:177], v[218:225], v[38:41], v190, v190 op_sel_hi:[0,0,0]
	v_mfma_scale_f32_16x16x128_f8f6f4 v[26:29], v[170:177], v[210:217], v[26:29], v190, v190 op_sel_hi:[0,0,0]
	v_mfma_scale_f32_16x16x128_f8f6f4 v[138:141], v[194:201], v[210:217], v[138:141], v190, v190 op_sel_hi:[0,0,0]
	v_mfma_scale_f32_16x16x128_f8f6f4 v[146:149], v[194:201], v[202:209], v[146:149], v190, v190 op_sel_hi:[0,0,0]
	v_mfma_scale_f32_16x16x128_f8f6f4 v[142:145], v[170:177], v[202:209], v[142:145], v190, v190 op_sel_hi:[0,0,0]
	s_setprio 0
	s_barrier
	s_mov_b32 m0, s9
	ds_read_b128 v[202:205], v191 offset:49152
	ds_read_b128 v[206:209], v191 offset:50176
	ds_read_b128 v[210:213], v191 offset:51200
	ds_read_b128 v[214:217], v191 offset:52224
	ds_read_b128 v[218:221], v191 offset:53248
	ds_read_b128 v[222:225], v191 offset:54272
	ds_read_b128 v[226:229], v191 offset:55296
	ds_read_b128 v[230:233], v191 offset:56320
	global_load_lds_dwordx4 v[72:73], off
	s_mov_b32 m0, s19
	s_nop 0
	global_load_lds_dwordx4 v[158:159], off
	s_mov_b32 m0, s44
	s_nop 0
	global_load_lds_dwordx4 v[162:163], off
	s_mov_b32 m0, s45
	s_nop 0
	global_load_lds_dwordx4 v[164:165], off
	s_mov_b32 m0, s18
	s_nop 0
	global_load_lds_dwordx4 v[70:71], off
	s_mov_b32 m0, s43
	s_nop 0
	global_load_lds_dwordx4 v[160:161], off
	s_waitcnt vmcnt(8)
	s_waitcnt lgkmcnt(0)
	s_barrier
	s_setprio 1
	s_waitcnt lgkmcnt(0)
	v_mfma_scale_f32_16x16x128_f8f6f4 v[134:137], v[2:9], v[202:209], v[134:137], v190, v190 op_sel_hi:[0,0,0]
	v_mfma_scale_f32_16x16x128_f8f6f4 v[102:105], v[10:17], v[202:209], v[102:105], v190, v190 op_sel_hi:[0,0,0]
	v_mfma_scale_f32_16x16x128_f8f6f4 v[98:101], v[10:17], v[210:217], v[98:101], v190, v190 op_sel_hi:[0,0,0]
	v_mfma_scale_f32_16x16x128_f8f6f4 v[122:125], v[2:9], v[210:217], v[122:125], v190, v190 op_sel_hi:[0,0,0]
	v_mfma_scale_f32_16x16x128_f8f6f4 v[110:113], v[2:9], v[218:225], v[110:113], v190, v190 op_sel_hi:[0,0,0]
	v_mfma_scale_f32_16x16x128_f8f6f4 v[106:109], v[10:17], v[218:225], v[106:109], v190, v190 op_sel_hi:[0,0,0]
	v_mfma_scale_f32_16x16x128_f8f6f4 v[82:85], v[10:17], v[226:233], v[82:85], v190, v190 op_sel_hi:[0,0,0]
	v_mfma_scale_f32_16x16x128_f8f6f4 v[86:89], v[2:9], v[226:233], v[86:89], v190, v190 op_sel_hi:[0,0,0]
	s_setprio 0
	s_setprio 1
	v_mfma_scale_f32_16x16x128_f8f6f4 v[54:57], v[170:177], v[226:233], v[54:57], v190, v190 op_sel_hi:[0,0,0]
	v_mfma_scale_f32_16x16x128_f8f6f4 v[58:61], v[194:201], v[226:233], v[58:61], v190, v190 op_sel_hi:[0,0,0]
	v_mfma_scale_f32_16x16x128_f8f6f4 v[94:97], v[194:201], v[218:225], v[94:97], v190, v190 op_sel_hi:[0,0,0]
	v_mfma_scale_f32_16x16x128_f8f6f4 v[66:69], v[170:177], v[218:225], v[66:69], v190, v190 op_sel_hi:[0,0,0]
	v_mfma_scale_f32_16x16x128_f8f6f4 v[46:49], v[170:177], v[210:217], v[46:49], v190, v190 op_sel_hi:[0,0,0]
	v_mfma_scale_f32_16x16x128_f8f6f4 v[118:121], v[194:201], v[210:217], v[118:121], v190, v190 op_sel_hi:[0,0,0]
	v_mfma_scale_f32_16x16x128_f8f6f4 v[130:133], v[194:201], v[202:209], v[130:133], v190, v190 op_sel_hi:[0,0,0]
	v_mfma_scale_f32_16x16x128_f8f6f4 v[34:37], v[170:177], v[202:209], v[34:37], v190, v190 op_sel_hi:[0,0,0]
	s_setprio 0
	s_barrier
	s_waitcnt vmcnt(0)
	s_cmpk_gt_u32 s65, 0xff
	s_cbranch_scc1 .LBB0_1439
	s_barrier

.LBB0_1558:
	s_add_u32 s39, s30, s38
	s_addc_u32 s44, s31, 0
	s_add_u32 s42, s39, 0x100
	s_addc_u32 s43, s44, 0
	s_and_b64 s[40:41], s[36:37], exec
	s_cselect_b32 s41, s18, s43
	s_cselect_b32 s40, s19, s42
	s_add_u32 s38, s28, s38
	s_addc_u32 s42, s29, 0
	s_add_u32 s38, s38, 0x100
	s_addc_u32 s42, s42, 0
	s_and_b64 s[36:37], s[36:37], exec
	s_cselect_b32 s43, s17, s42
	s_cselect_b32 s42, s21, s38
	s_add_u32 s76, s39, 0x10080
	ds_read_b128 v[26:29], v181
	ds_read_b128 v[30:33], v181 offset:1024
	ds_read_b128 v[18:21], v181 offset:2048
	ds_read_b128 v[22:25], v181 offset:3072
	ds_read_b128 v[10:13], v182
	ds_read_b128 v[14:17], v182 offset:1024
	ds_read_b128 v[2:5], v182 offset:2048
	ds_read_b128 v[6:9], v182 offset:3072
	s_addc_u32 s77, s44, 0
	s_add_i32 s75, s63, s15
	s_add_i32 m0, s27, 0xc000
	s_add_i32 s78, s27, 0xe000
	s_add_i32 s72, s75, 0x2000
	s_add_u32 s44, s42, 0x10000
	s_addc_u32 s45, s43, 0
	s_add_i32 s74, s64, s15
	s_add_i32 s73, s74, 0x2000
	s_add_i32 s71, 0, 0x18000
	s_add_i32 s70, 0, 0x1c000
	s_add_u32 s38, s40, 0x10000
	s_addc_u32 s39, s41, 0
	s_add_i32 s69, s71, s15
	s_add_i32 s67, s69, 0x2000
	s_add_u32 s36, s42, 0x10080
	s_addc_u32 s37, s43, 0
	s_add_i32 s68, s70, s15
	s_add_i32 s66, s68, 0x2000
	v_lshl_add_u64 v[208:209], s[76:77], 0, v[164:165]
	ds_read_b128 v[170:173], v183
	ds_read_b128 v[174:177], v183 offset:1024
	ds_read_b128 v[184:187], v183 offset:2048
	ds_read_b128 v[188:191], v183 offset:3072
	ds_read_b128 v[192:195], v183 offset:4096
	ds_read_b128 v[196:199], v183 offset:5120
	ds_read_b128 v[200:203], v183 offset:6144
	ds_read_b128 v[204:207], v183 offset:7168
	global_load_lds_dwordx4 v[208:209], off
	v_lshl_add_u64 v[208:209], s[76:77], 0, v[162:163]
	s_mov_b32 m0, s78
	s_nop 0
	global_load_lds_dwordx4 v[208:209], off
	s_waitcnt vmcnt(8)
	s_waitcnt lgkmcnt(0)
	s_barrier
	s_setprio 1
	s_waitcnt lgkmcnt(0)
	v_mfma_scale_f32_16x16x128_f8f6f4 v[158:161], v[26:33], v[170:177], v[158:161], v1, v1 op_sel_hi:[0,0,0]
	v_mfma_scale_f32_16x16x128_f8f6f4 v[154:157], v[18:25], v[170:177], v[154:157], v1, v1 op_sel_hi:[0,0,0]
	v_mfma_scale_f32_16x16x128_f8f6f4 v[138:141], v[18:25], v[184:191], v[138:141], v1, v1 op_sel_hi:[0,0,0]
	v_mfma_scale_f32_16x16x128_f8f6f4 v[142:145], v[26:33], v[184:191], v[142:145], v1, v1 op_sel_hi:[0,0,0]
	v_mfma_scale_f32_16x16x128_f8f6f4 v[126:129], v[26:33], v[192:199], v[126:129], v1, v1 op_sel_hi:[0,0,0]
	v_mfma_scale_f32_16x16x128_f8f6f4 v[122:125], v[18:25], v[192:199], v[122:125], v1, v1 op_sel_hi:[0,0,0]
	v_mfma_scale_f32_16x16x128_f8f6f4 v[106:109], v[18:25], v[200:207], v[106:109], v1, v1 op_sel_hi:[0,0,0]
	v_mfma_scale_f32_16x16x128_f8f6f4 v[110:113], v[26:33], v[200:207], v[110:113], v1, v1 op_sel_hi:[0,0,0]
	s_setprio 0
	s_setprio 1
	v_mfma_scale_f32_16x16x128_f8f6f4 v[102:105], v[10:17], v[200:207], v[102:105], v1, v1 op_sel_hi:[0,0,0]
	v_mfma_scale_f32_16x16x128_f8f6f4 v[98:101], v[2:9], v[200:207], v[98:101], v1, v1 op_sel_hi:[0,0,0]
	v_mfma_scale_f32_16x16x128_f8f6f4 v[114:117], v[2:9], v[192:199], v[114:117], v1, v1 op_sel_hi:[0,0,0]
	v_mfma_scale_f32_16x16x128_f8f6f4 v[118:121], v[10:17], v[192:199], v[118:121], v1, v1 op_sel_hi:[0,0,0]
	v_mfma_scale_f32_16x16x128_f8f6f4 v[134:137], v[10:17], v[184:191], v[134:137], v1, v1 op_sel_hi:[0,0,0]
	v_mfma_scale_f32_16x16x128_f8f6f4 v[130:133], v[2:9], v[184:191], v[130:133], v1, v1 op_sel_hi:[0,0,0]
	v_mfma_scale_f32_16x16x128_f8f6f4 v[146:149], v[2:9], v[170:177], v[146:149], v1, v1 op_sel_hi:[0,0,0]
	v_mfma_scale_f32_16x16x128_f8f6f4 v[150:153], v[10:17], v[170:177], v[150:153], v1, v1 op_sel_hi:[0,0,0]
	s_setprio 0
	s_barrier
	s_mov_b32 m0, s75
	v_lshl_add_u64 v[170:171], s[42:43], 0, v[164:165]
	ds_read_b128 v[184:187], v183 offset:16384
	ds_read_b128 v[188:191], v183 offset:17408
	ds_read_b128 v[192:195], v183 offset:18432
	ds_read_b128 v[196:199], v183 offset:19456
	ds_read_b128 v[200:203], v183 offset:20480
	ds_read_b128 v[204:207], v183 offset:21504
	ds_read_b128 v[208:211], v183 offset:22528
	ds_read_b128 v[212:215], v183 offset:23552
	global_load_lds_dwordx4 v[170:171], off
	v_lshl_add_u64 v[172:173], s[42:43], 0, v[162:163]
	s_mov_b32 m0, s72
	v_lshl_add_u64 v[174:175], s[44:45], 0, v[164:165]
	global_load_lds_dwordx4 v[172:173], off
	s_mov_b32 m0, s74
	v_lshl_add_u64 v[176:177], s[40:41], 0, v[162:163]
	global_load_lds_dwordx4 v[174:175], off
	v_lshl_add_u64 v[174:175], s[44:45], 0, v[162:163]
	s_mov_b32 m0, s73
	s_nop 0
	global_load_lds_dwordx4 v[174:175], off
	v_lshl_add_u64 v[174:175], s[40:41], 0, v[164:165]
	s_mov_b32 m0, s27
	s_nop 0
	global_load_lds_dwordx4 v[174:175], off
	s_mov_b32 m0, s49
	s_nop 0
	global_load_lds_dwordx4 v[176:177], off
	s_waitcnt vmcnt(8)
	s_waitcnt lgkmcnt(0)
	s_barrier
	s_setprio 1
	s_waitcnt lgkmcnt(0)
	v_mfma_scale_f32_16x16x128_f8f6f4 v[94:97], v[26:33], v[184:191], v[94:97], v1, v1 op_sel_hi:[0,0,0]
	v_mfma_scale_f32_16x16x128_f8f6f4 v[90:93], v[18:25], v[184:191], v[90:93], v1, v1 op_sel_hi:[0,0,0]
	v_mfma_scale_f32_16x16x128_f8f6f4 v[74:77], v[18:25], v[192:199], v[74:77], v1, v1 op_sel_hi:[0,0,0]
	v_mfma_scale_f32_16x16x128_f8f6f4 v[78:81], v[26:33], v[192:199], v[78:81], v1, v1 op_sel_hi:[0,0,0]
	v_mfma_scale_f32_16x16x128_f8f6f4 v[62:65], v[26:33], v[200:207], v[62:65], v1, v1 op_sel_hi:[0,0,0]
	v_mfma_scale_f32_16x16x128_f8f6f4 v[58:61], v[18:25], v[200:207], v[58:61], v1, v1 op_sel_hi:[0,0,0]
	v_mfma_scale_f32_16x16x128_f8f6f4 v[42:45], v[18:25], v[208:215], v[42:45], v1, v1 op_sel_hi:[0,0,0]
	v_mfma_scale_f32_16x16x128_f8f6f4 v[54:57], v[26:33], v[208:215], v[54:57], v1, v1 op_sel_hi:[0,0,0]
	s_setprio 0
	s_setprio 1
	v_mfma_scale_f32_16x16x128_f8f6f4 v[38:41], v[10:17], v[208:215], v[38:41], v1, v1 op_sel_hi:[0,0,0]
	v_mfma_scale_f32_16x16x128_f8f6f4 v[34:37], v[2:9], v[208:215], v[34:37], v1, v1 op_sel_hi:[0,0,0]
	v_mfma_scale_f32_16x16x128_f8f6f4 v[46:49], v[2:9], v[200:207], v[46:49], v1, v1 op_sel_hi:[0,0,0]
	v_mfma_scale_f32_16x16x128_f8f6f4 v[50:53], v[10:17], v[200:207], v[50:53], v1, v1 op_sel_hi:[0,0,0]
	v_mfma_scale_f32_16x16x128_f8f6f4 v[70:73], v[10:17], v[192:199], v[70:73], v1, v1 op_sel_hi:[0,0,0]
	v_mfma_scale_f32_16x16x128_f8f6f4 v[66:69], v[2:9], v[192:199], v[66:69], v1, v1 op_sel_hi:[0,0,0]
	v_mfma_scale_f32_16x16x128_f8f6f4 v[82:85], v[2:9], v[184:191], v[82:85], v1, v1 op_sel_hi:[0,0,0]
	v_mfma_scale_f32_16x16x128_f8f6f4 v[86:89], v[10:17], v[184:191], v[86:89], v1, v1 op_sel_hi:[0,0,0]
	s_setprio 0
	s_barrier
	v_add_u32_e32 v14, s71, v179
	v_add_u32_e32 v30, s70, v179
	ds_read_b128 v[2:5], v14
	ds_read_b128 v[6:9], v14 offset:1024
	ds_read_b128 v[10:13], v14 offset:2048
	ds_read_b128 v[14:17], v14 offset:3072
	ds_read_b128 v[18:21], v30
	ds_read_b128 v[22:25], v30 offset:1024
	ds_read_b128 v[26:29], v30 offset:2048
	ds_read_b128 v[30:33], v30 offset:3072
	s_mov_b32 m0, s50
	v_lshl_add_u64 v[216:217], s[38:39], 0, v[164:165]
	ds_read_b128 v[184:187], v183 offset:32768
	ds_read_b128 v[188:191], v183 offset:33792
	ds_read_b128 v[192:195], v183 offset:34816
	ds_read_b128 v[196:199], v183 offset:35840
	ds_read_b128 v[200:203], v183 offset:36864
	ds_read_b128 v[204:207], v183 offset:37888
	ds_read_b128 v[208:211], v183 offset:38912
	ds_read_b128 v[212:215], v183 offset:39936
	global_load_lds_dwordx4 v[216:217], off
	v_lshl_add_u64 v[216:217], s[38:39], 0, v[162:163]
	s_mov_b32 m0, s51
	s_nop 0
	global_load_lds_dwordx4 v[216:217], off
	s_waitcnt vmcnt(8)
	s_waitcnt lgkmcnt(0)
	s_barrier
	s_setprio 1
	s_waitcnt lgkmcnt(0)
	v_mfma_scale_f32_16x16x128_f8f6f4 v[158:161], v[2:9], v[184:191], v[158:161], v1, v1 op_sel_hi:[0,0,0]
	v_mfma_scale_f32_16x16x128_f8f6f4 v[154:157], v[10:17], v[184:191], v[154:157], v1, v1 op_sel_hi:[0,0,0]
	v_mfma_scale_f32_16x16x128_f8f6f4 v[138:141], v[10:17], v[192:199], v[138:141], v1, v1 op_sel_hi:[0,0,0]
	v_mfma_scale_f32_16x16x128_f8f6f4 v[142:145], v[2:9], v[192:199], v[142:145], v1, v1 op_sel_hi:[0,0,0]
	v_mfma_scale_f32_16x16x128_f8f6f4 v[126:129], v[2:9], v[200:207], v[126:129], v1, v1 op_sel_hi:[0,0,0]
	v_mfma_scale_f32_16x16x128_f8f6f4 v[122:125], v[10:17], v[200:207], v[122:125], v1, v1 op_sel_hi:[0,0,0]
	v_mfma_scale_f32_16x16x128_f8f6f4 v[106:109], v[10:17], v[208:215], v[106:109], v1, v1 op_sel_hi:[0,0,0]
	v_mfma_scale_f32_16x16x128_f8f6f4 v[110:113], v[2:9], v[208:215], v[110:113], v1, v1 op_sel_hi:[0,0,0]
	s_setprio 0
	s_setprio 1
	v_mfma_scale_f32_16x16x128_f8f6f4 v[102:105], v[18:25], v[208:215], v[102:105], v1, v1 op_sel_hi:[0,0,0]
	v_mfma_scale_f32_16x16x128_f8f6f4 v[98:101], v[26:33], v[208:215], v[98:101], v1, v1 op_sel_hi:[0,0,0]
	v_mfma_scale_f32_16x16x128_f8f6f4 v[114:117], v[26:33], v[200:207], v[114:117], v1, v1 op_sel_hi:[0,0,0]
	v_mfma_scale_f32_16x16x128_f8f6f4 v[118:121], v[18:25], v[200:207], v[118:121], v1, v1 op_sel_hi:[0,0,0]
	v_mfma_scale_f32_16x16x128_f8f6f4 v[134:137], v[18:25], v[192:199], v[134:137], v1, v1 op_sel_hi:[0,0,0]
	v_mfma_scale_f32_16x16x128_f8f6f4 v[130:133], v[26:33], v[192:199], v[130:133], v1, v1 op_sel_hi:[0,0,0]
	v_mfma_scale_f32_16x16x128_f8f6f4 v[146:149], v[26:33], v[184:191], v[146:149], v1, v1 op_sel_hi:[0,0,0]
	v_mfma_scale_f32_16x16x128_f8f6f4 v[150:153], v[18:25], v[184:191], v[150:153], v1, v1 op_sel_hi:[0,0,0]
	s_setprio 0
	s_barrier
	s_mov_b32 m0, s69
	v_lshl_add_u64 v[170:171], v[170:171], 0, s[8:9]
	ds_read_b128 v[184:187], v183 offset:49152
	ds_read_b128 v[188:191], v183 offset:50176
	ds_read_b128 v[192:195], v183 offset:51200
	ds_read_b128 v[196:199], v183 offset:52224
	ds_read_b128 v[200:203], v183 offset:53248
	ds_read_b128 v[204:207], v183 offset:54272
	ds_read_b128 v[208:211], v183 offset:55296
	ds_read_b128 v[212:215], v183 offset:56320
	global_load_lds_dwordx4 v[170:171], off
	v_lshl_add_u64 v[170:171], v[172:173], 0, s[8:9]
	s_mov_b32 m0, s67
	s_nop 0
	global_load_lds_dwordx4 v[170:171], off
	v_lshl_add_u64 v[170:171], s[36:37], 0, v[164:165]
	s_mov_b32 m0, s68
	s_nop 0
	global_load_lds_dwordx4 v[170:171], off
	v_lshl_add_u64 v[170:171], s[36:37], 0, v[162:163]
	s_mov_b32 m0, s66
	s_nop 0
	global_load_lds_dwordx4 v[170:171], off
	v_lshl_add_u64 v[170:171], v[174:175], 0, s[8:9]
	s_mov_b32 m0, s61
	s_nop 0
	global_load_lds_dwordx4 v[170:171], off
	v_lshl_add_u64 v[170:171], v[176:177], 0, s[8:9]
	s_mov_b32 m0, s62
	s_nop 0
	global_load_lds_dwordx4 v[170:171], off
	s_waitcnt vmcnt(8)
	s_waitcnt lgkmcnt(0)
	s_barrier
	s_setprio 1
	s_waitcnt lgkmcnt(0)
	v_mfma_scale_f32_16x16x128_f8f6f4 v[94:97], v[2:9], v[184:191], v[94:97], v1, v1 op_sel_hi:[0,0,0]
	v_mfma_scale_f32_16x16x128_f8f6f4 v[90:93], v[10:17], v[184:191], v[90:93], v1, v1 op_sel_hi:[0,0,0]
	v_mfma_scale_f32_16x16x128_f8f6f4 v[74:77], v[10:17], v[192:199], v[74:77], v1, v1 op_sel_hi:[0,0,0]
	v_mfma_scale_f32_16x16x128_f8f6f4 v[78:81], v[2:9], v[192:199], v[78:81], v1, v1 op_sel_hi:[0,0,0]
	v_mfma_scale_f32_16x16x128_f8f6f4 v[62:65], v[2:9], v[200:207], v[62:65], v1, v1 op_sel_hi:[0,0,0]
	v_mfma_scale_f32_16x16x128_f8f6f4 v[58:61], v[10:17], v[200:207], v[58:61], v1, v1 op_sel_hi:[0,0,0]
	v_mfma_scale_f32_16x16x128_f8f6f4 v[42:45], v[10:17], v[208:215], v[42:45], v1, v1 op_sel_hi:[0,0,0]
	v_mfma_scale_f32_16x16x128_f8f6f4 v[54:57], v[2:9], v[208:215], v[54:57], v1, v1 op_sel_hi:[0,0,0]
	s_setprio 0
	s_setprio 1
	v_mfma_scale_f32_16x16x128_f8f6f4 v[38:41], v[18:25], v[208:215], v[38:41], v1, v1 op_sel_hi:[0,0,0]
	v_mfma_scale_f32_16x16x128_f8f6f4 v[34:37], v[26:33], v[208:215], v[34:37], v1, v1 op_sel_hi:[0,0,0]
	v_mfma_scale_f32_16x16x128_f8f6f4 v[46:49], v[26:33], v[200:207], v[46:49], v1, v1 op_sel_hi:[0,0,0]
	v_mfma_scale_f32_16x16x128_f8f6f4 v[50:53], v[18:25], v[200:207], v[50:53], v1, v1 op_sel_hi:[0,0,0]
	v_mfma_scale_f32_16x16x128_f8f6f4 v[70:73], v[18:25], v[192:199], v[70:73], v1, v1 op_sel_hi:[0,0,0]
	v_mfma_scale_f32_16x16x128_f8f6f4 v[66:69], v[26:33], v[192:199], v[66:69], v1, v1 op_sel_hi:[0,0,0]
	v_mfma_scale_f32_16x16x128_f8f6f4 v[82:85], v[26:33], v[184:191], v[82:85], v1, v1 op_sel_hi:[0,0,0]
	v_mfma_scale_f32_16x16x128_f8f6f4 v[86:89], v[18:25], v[184:191], v[86:89], v1, v1 op_sel_hi:[0,0,0]
	s_setprio 0
	s_barrier
	s_movk_i32 s38, 0x100
	s_andn2_b64 vcc, exec, s[34:35]
	s_mov_b64 s[36:37], -1
	s_mov_b64 s[34:35], 0
	s_cbranch_vccz .LBB0_1558
	s_and_b64 vcc, exec, s[12:13]
	s_cbranch_vccz .LBB0_1561
	s_barrier

.LBB0_1681:
	ds_read_b128 v[26:29], v189
	ds_read_b128 v[30:33], v189 offset:1024
	ds_read_b128 v[18:21], v189 offset:2048
	ds_read_b128 v[22:25], v189 offset:3072
	ds_read_b128 v[10:13], v190
	ds_read_b128 v[14:17], v190 offset:1024
	ds_read_b128 v[2:5], v190 offset:2048
	ds_read_b128 v[6:9], v190 offset:3072
	s_add_u32 s34, s30, 0xfff80080
	s_addc_u32 s35, s31, -1
	s_cmp_eq_u32 s60, 28
	s_cselect_b32 s37, s18, s35
	s_cselect_b32 s36, s19, s34
	s_cselect_b32 s35, s21, s59
	s_cselect_b32 s34, s23, s58
	s_mov_b32 m0, s43
	s_nop 0
	global_load_lds_dwordx4 v168, s[100:101]
	s_mov_b32 m0, s44
	s_nop 0
	global_load_lds_dwordx4 v164, s[100:101]
	s_add_i32 m0, s29, 0xc000
	ds_read_b128 v[178:181], v191
	ds_read_b128 v[182:185], v191 offset:1024
	ds_read_b128 v[194:197], v191 offset:2048
	ds_read_b128 v[198:201], v191 offset:3072
	ds_read_b128 v[202:205], v191 offset:4096
	ds_read_b128 v[206:209], v191 offset:5120
	ds_read_b128 v[210:213], v191 offset:6144
	ds_read_b128 v[214:217], v191 offset:7168
	global_load_lds_dwordx4 v170, s[30:31]
	s_add_i32 m0, s29, 0xe000
	s_nop 0
	global_load_lds_dwordx4 v172, s[30:31]
	s_waitcnt vmcnt(8)
	s_waitcnt lgkmcnt(0)
	s_barrier
	s_setprio 1
	s_waitcnt lgkmcnt(0)
	v_mfma_scale_f32_16x16x128_f8f6f4 v[158:161], v[26:33], v[178:185], v[158:161], v1, v1 op_sel_hi:[0,0,0]
	v_mfma_scale_f32_16x16x128_f8f6f4 v[154:157], v[18:25], v[178:185], v[154:157], v1, v1 op_sel_hi:[0,0,0]
	v_mfma_scale_f32_16x16x128_f8f6f4 v[138:141], v[18:25], v[194:201], v[138:141], v1, v1 op_sel_hi:[0,0,0]
	v_mfma_scale_f32_16x16x128_f8f6f4 v[142:145], v[26:33], v[194:201], v[142:145], v1, v1 op_sel_hi:[0,0,0]
	v_mfma_scale_f32_16x16x128_f8f6f4 v[126:129], v[26:33], v[202:209], v[126:129], v1, v1 op_sel_hi:[0,0,0]
	v_mfma_scale_f32_16x16x128_f8f6f4 v[122:125], v[18:25], v[202:209], v[122:125], v1, v1 op_sel_hi:[0,0,0]
	v_mfma_scale_f32_16x16x128_f8f6f4 v[106:109], v[18:25], v[210:217], v[106:109], v1, v1 op_sel_hi:[0,0,0]
	v_mfma_scale_f32_16x16x128_f8f6f4 v[110:113], v[26:33], v[210:217], v[110:113], v1, v1 op_sel_hi:[0,0,0]
	s_setprio 0
	s_setprio 1
	v_mfma_scale_f32_16x16x128_f8f6f4 v[102:105], v[10:17], v[210:217], v[102:105], v1, v1 op_sel_hi:[0,0,0]
	v_mfma_scale_f32_16x16x128_f8f6f4 v[98:101], v[2:9], v[210:217], v[98:101], v1, v1 op_sel_hi:[0,0,0]
	v_mfma_scale_f32_16x16x128_f8f6f4 v[114:117], v[2:9], v[202:209], v[114:117], v1, v1 op_sel_hi:[0,0,0]
	v_mfma_scale_f32_16x16x128_f8f6f4 v[118:121], v[10:17], v[202:209], v[118:121], v1, v1 op_sel_hi:[0,0,0]
	v_mfma_scale_f32_16x16x128_f8f6f4 v[134:137], v[10:17], v[194:201], v[134:137], v1, v1 op_sel_hi:[0,0,0]
	v_mfma_scale_f32_16x16x128_f8f6f4 v[130:133], v[2:9], v[194:201], v[130:133], v1, v1 op_sel_hi:[0,0,0]
	v_mfma_scale_f32_16x16x128_f8f6f4 v[146:149], v[2:9], v[178:185], v[146:149], v1, v1 op_sel_hi:[0,0,0]
	v_mfma_scale_f32_16x16x128_f8f6f4 v[150:153], v[10:17], v[178:185], v[150:153], v1, v1 op_sel_hi:[0,0,0]
	s_setprio 0
	s_barrier
	s_add_i32 s61, s45, s3
	s_mov_b32 m0, s61
	ds_read_b128 v[194:197], v191 offset:16384
	ds_read_b128 v[198:201], v191 offset:17408
	ds_read_b128 v[202:205], v191 offset:18432
	ds_read_b128 v[206:209], v191 offset:19456
	ds_read_b128 v[210:213], v191 offset:20480
	ds_read_b128 v[214:217], v191 offset:21504
	ds_read_b128 v[218:221], v191 offset:22528
	ds_read_b128 v[222:225], v191 offset:23552
	global_load_lds_dwordx4 v166, s[34:35]
	s_add_i32 m0, s61, 0x2000
	s_add_u32 s62, s34, 0x80000
	s_addc_u32 s63, s35, 0
	s_add_i32 s61, s48, s3
	global_load_lds_dwordx4 v162, s[34:35]
	s_mov_b32 m0, s61
	s_nop 0
	global_load_lds_dwordx4 v166, s[62:63]
	s_add_i32 m0, s61, 0x2000
	s_nop 0
	global_load_lds_dwordx4 v162, s[62:63]
	s_waitcnt vmcnt(6)
	s_waitcnt lgkmcnt(0)
	s_barrier
	s_setprio 1
	s_waitcnt lgkmcnt(0)
	v_mfma_scale_f32_16x16x128_f8f6f4 v[94:97], v[26:33], v[194:201], v[94:97], v1, v1 op_sel_hi:[0,0,0]
	v_mfma_scale_f32_16x16x128_f8f6f4 v[90:93], v[18:25], v[194:201], v[90:93], v1, v1 op_sel_hi:[0,0,0]
	v_mfma_scale_f32_16x16x128_f8f6f4 v[74:77], v[18:25], v[202:209], v[74:77], v1, v1 op_sel_hi:[0,0,0]
	v_mfma_scale_f32_16x16x128_f8f6f4 v[78:81], v[26:33], v[202:209], v[78:81], v1, v1 op_sel_hi:[0,0,0]
	v_mfma_scale_f32_16x16x128_f8f6f4 v[62:65], v[26:33], v[210:217], v[62:65], v1, v1 op_sel_hi:[0,0,0]
	v_mfma_scale_f32_16x16x128_f8f6f4 v[58:61], v[18:25], v[210:217], v[58:61], v1, v1 op_sel_hi:[0,0,0]
	v_mfma_scale_f32_16x16x128_f8f6f4 v[42:45], v[18:25], v[218:225], v[42:45], v1, v1 op_sel_hi:[0,0,0]
	v_mfma_scale_f32_16x16x128_f8f6f4 v[46:49], v[26:33], v[218:225], v[46:49], v1, v1 op_sel_hi:[0,0,0]
	s_setprio 0
	s_setprio 1
	v_mfma_scale_f32_16x16x128_f8f6f4 v[38:41], v[10:17], v[218:225], v[38:41], v1, v1 op_sel_hi:[0,0,0]
	v_mfma_scale_f32_16x16x128_f8f6f4 v[34:37], v[2:9], v[218:225], v[34:37], v1, v1 op_sel_hi:[0,0,0]
	v_mfma_scale_f32_16x16x128_f8f6f4 v[50:53], v[2:9], v[210:217], v[50:53], v1, v1 op_sel_hi:[0,0,0]
	v_mfma_scale_f32_16x16x128_f8f6f4 v[54:57], v[10:17], v[210:217], v[54:57], v1, v1 op_sel_hi:[0,0,0]
	v_mfma_scale_f32_16x16x128_f8f6f4 v[70:73], v[10:17], v[202:209], v[70:73], v1, v1 op_sel_hi:[0,0,0]
	v_mfma_scale_f32_16x16x128_f8f6f4 v[66:69], v[2:9], v[202:209], v[66:69], v1, v1 op_sel_hi:[0,0,0]
	v_mfma_scale_f32_16x16x128_f8f6f4 v[82:85], v[2:9], v[194:201], v[82:85], v1, v1 op_sel_hi:[0,0,0]
	v_mfma_scale_f32_16x16x128_f8f6f4 v[86:89], v[10:17], v[194:201], v[86:89], v1, v1 op_sel_hi:[0,0,0]
	s_setprio 0
	s_barrier
	s_add_i32 s61, 0, 0x18000
	s_add_i32 s62, 0, 0x1c000
	v_add_u32_e32 v14, s61, v187
	v_add_u32_e32 v30, s62, v187
	ds_read_b128 v[2:5], v14
	ds_read_b128 v[6:9], v14 offset:1024
	ds_read_b128 v[10:13], v14 offset:2048
	ds_read_b128 v[14:17], v14 offset:3072
	ds_read_b128 v[18:21], v30
	ds_read_b128 v[22:25], v30 offset:1024
	ds_read_b128 v[26:29], v30 offset:2048
	ds_read_b128 v[30:33], v30 offset:3072
	s_mov_b32 m0, s29
	s_nop 0
	global_load_lds_dwordx4 v168, s[36:37]
	s_mov_b32 m0, s38
	s_nop 0
	global_load_lds_dwordx4 v164, s[36:37]
	s_add_u32 s36, s36, 0x80000
	s_addc_u32 s37, s37, 0
	s_add_u32 s100, s36, 0xfff80080
	s_addc_u32 s101, s37, -1
	s_mov_b32 m0, s39
	ds_read_b128 v[194:197], v191 offset:32768
	ds_read_b128 v[198:201], v191 offset:33792
	ds_read_b128 v[202:205], v191 offset:34816
	ds_read_b128 v[206:209], v191 offset:35840
	ds_read_b128 v[210:213], v191 offset:36864
	ds_read_b128 v[214:217], v191 offset:37888
	ds_read_b128 v[218:221], v191 offset:38912
	ds_read_b128 v[222:225], v191 offset:39936
	global_load_lds_dwordx4 v168, s[36:37]
	s_mov_b32 m0, s40
	s_nop 0
	global_load_lds_dwordx4 v164, s[36:37]
	s_waitcnt vmcnt(8)
	s_waitcnt lgkmcnt(0)
	s_barrier
	s_setprio 1
	s_waitcnt lgkmcnt(0)
	v_mfma_scale_f32_16x16x128_f8f6f4 v[158:161], v[2:9], v[194:201], v[158:161], v1, v1 op_sel_hi:[0,0,0]
	v_mfma_scale_f32_16x16x128_f8f6f4 v[154:157], v[10:17], v[194:201], v[154:157], v1, v1 op_sel_hi:[0,0,0]
	v_mfma_scale_f32_16x16x128_f8f6f4 v[138:141], v[10:17], v[202:209], v[138:141], v1, v1 op_sel_hi:[0,0,0]
	v_mfma_scale_f32_16x16x128_f8f6f4 v[142:145], v[2:9], v[202:209], v[142:145], v1, v1 op_sel_hi:[0,0,0]
	v_mfma_scale_f32_16x16x128_f8f6f4 v[126:129], v[2:9], v[210:217], v[126:129], v1, v1 op_sel_hi:[0,0,0]
	v_mfma_scale_f32_16x16x128_f8f6f4 v[122:125], v[10:17], v[210:217], v[122:125], v1, v1 op_sel_hi:[0,0,0]
	v_mfma_scale_f32_16x16x128_f8f6f4 v[106:109], v[10:17], v[218:225], v[106:109], v1, v1 op_sel_hi:[0,0,0]
	v_mfma_scale_f32_16x16x128_f8f6f4 v[110:113], v[2:9], v[218:225], v[110:113], v1, v1 op_sel_hi:[0,0,0]
	s_setprio 0
	s_setprio 1
	v_mfma_scale_f32_16x16x128_f8f6f4 v[102:105], v[18:25], v[218:225], v[102:105], v1, v1 op_sel_hi:[0,0,0]
	v_mfma_scale_f32_16x16x128_f8f6f4 v[98:101], v[26:33], v[218:225], v[98:101], v1, v1 op_sel_hi:[0,0,0]
	v_mfma_scale_f32_16x16x128_f8f6f4 v[114:117], v[26:33], v[210:217], v[114:117], v1, v1 op_sel_hi:[0,0,0]
	v_mfma_scale_f32_16x16x128_f8f6f4 v[118:121], v[18:25], v[210:217], v[118:121], v1, v1 op_sel_hi:[0,0,0]
	v_mfma_scale_f32_16x16x128_f8f6f4 v[134:137], v[18:25], v[202:209], v[134:137], v1, v1 op_sel_hi:[0,0,0]
	v_mfma_scale_f32_16x16x128_f8f6f4 v[130:133], v[26:33], v[202:209], v[130:133], v1, v1 op_sel_hi:[0,0,0]
	v_mfma_scale_f32_16x16x128_f8f6f4 v[146:149], v[26:33], v[194:201], v[146:149], v1, v1 op_sel_hi:[0,0,0]
	v_mfma_scale_f32_16x16x128_f8f6f4 v[150:153], v[18:25], v[194:201], v[150:153], v1, v1 op_sel_hi:[0,0,0]
	s_setprio 0
	s_barrier
	s_add_i32 s36, s61, s3
	s_mov_b32 m0, s36
	s_add_u32 s98, s34, 0x80
	s_addc_u32 s99, s35, 0
	ds_read_b128 v[194:197], v191 offset:49152
	ds_read_b128 v[198:201], v191 offset:50176
	ds_read_b128 v[202:205], v191 offset:51200
	ds_read_b128 v[206:209], v191 offset:52224
	ds_read_b128 v[210:213], v191 offset:53248
	ds_read_b128 v[214:217], v191 offset:54272
	ds_read_b128 v[218:221], v191 offset:55296
	ds_read_b128 v[222:225], v191 offset:56320
	global_load_lds_dwordx4 v166, s[98:99]
	s_add_i32 m0, s36, 0x2000
	s_add_u32 s34, s34, 0x80080
	s_addc_u32 s35, s35, 0
	s_add_i32 s36, s62, s3
	global_load_lds_dwordx4 v162, s[98:99]
	s_mov_b32 m0, s36
	s_nop 0
	global_load_lds_dwordx4 v166, s[34:35]
	s_add_i32 m0, s36, 0x2000
	s_nop 0
	global_load_lds_dwordx4 v162, s[34:35]
	s_waitcnt vmcnt(6)
	s_waitcnt lgkmcnt(0)
	s_barrier
	s_setprio 1
	s_waitcnt lgkmcnt(0)
	v_mfma_scale_f32_16x16x128_f8f6f4 v[94:97], v[2:9], v[194:201], v[94:97], v1, v1 op_sel_hi:[0,0,0]
	v_mfma_scale_f32_16x16x128_f8f6f4 v[90:93], v[10:17], v[194:201], v[90:93], v1, v1 op_sel_hi:[0,0,0]
	v_mfma_scale_f32_16x16x128_f8f6f4 v[74:77], v[10:17], v[202:209], v[74:77], v1, v1 op_sel_hi:[0,0,0]
	v_mfma_scale_f32_16x16x128_f8f6f4 v[78:81], v[2:9], v[202:209], v[78:81], v1, v1 op_sel_hi:[0,0,0]
	v_mfma_scale_f32_16x16x128_f8f6f4 v[62:65], v[2:9], v[210:217], v[62:65], v1, v1 op_sel_hi:[0,0,0]
	v_mfma_scale_f32_16x16x128_f8f6f4 v[58:61], v[10:17], v[210:217], v[58:61], v1, v1 op_sel_hi:[0,0,0]
	v_mfma_scale_f32_16x16x128_f8f6f4 v[42:45], v[10:17], v[218:225], v[42:45], v1, v1 op_sel_hi:[0,0,0]
	v_mfma_scale_f32_16x16x128_f8f6f4 v[46:49], v[2:9], v[218:225], v[46:49], v1, v1 op_sel_hi:[0,0,0]
	s_setprio 0
	s_setprio 1
	v_mfma_scale_f32_16x16x128_f8f6f4 v[38:41], v[18:25], v[218:225], v[38:41], v1, v1 op_sel_hi:[0,0,0]
	v_mfma_scale_f32_16x16x128_f8f6f4 v[34:37], v[26:33], v[218:225], v[34:37], v1, v1 op_sel_hi:[0,0,0]
	v_mfma_scale_f32_16x16x128_f8f6f4 v[50:53], v[26:33], v[210:217], v[50:53], v1, v1 op_sel_hi:[0,0,0]
	v_mfma_scale_f32_16x16x128_f8f6f4 v[54:57], v[18:25], v[210:217], v[54:57], v1, v1 op_sel_hi:[0,0,0]
	v_mfma_scale_f32_16x16x128_f8f6f4 v[70:73], v[18:25], v[202:209], v[70:73], v1, v1 op_sel_hi:[0,0,0]
	v_mfma_scale_f32_16x16x128_f8f6f4 v[66:69], v[26:33], v[202:209], v[66:69], v1, v1 op_sel_hi:[0,0,0]
	v_mfma_scale_f32_16x16x128_f8f6f4 v[82:85], v[26:33], v[194:201], v[82:85], v1, v1 op_sel_hi:[0,0,0]
	v_mfma_scale_f32_16x16x128_f8f6f4 v[86:89], v[18:25], v[194:201], v[86:89], v1, v1 op_sel_hi:[0,0,0]
	s_setprio 0
	s_barrier
	s_add_i32 s60, s60, 2
	s_add_u32 s30, s30, 0x100
	s_addc_u32 s31, s31, 0
	s_add_u32 s58, s58, 0x100
	s_addc_u32 s59, s59, 0
	s_cmp_gt_u32 s60, 29
	s_cbranch_scc0 .LBB0_1681
	s_and_b64 vcc, exec, s[12:13]
	s_cbranch_vccz .LBB0_1684
	s_barrier

.LBB0_1745:
	s_add_u32 s8, s49, s6
	s_addc_u32 s9, s50, s7
	s_add_u32 s8, s8, 0x32800100
	s_addc_u32 s9, s9, 0
	s_add_u32 s73, s51, s6
	s_addc_u32 s74, s54, s7
	s_add_i32 s72, 0, 0x10000
	s_cmpk_eq_i32 s6, 0x2a00
	s_cselect_b32 s37, s5, s9
	s_cselect_b32 s36, s4, s8
	s_cselect_b32 s9, s13, s74
	s_cselect_b32 s8, s12, s73
	s_add_i32 s73, 0, 0x14000
	v_add_u32_e32 v2, s72, v188
	v_add_u32_e32 v6, s73, v188
	ds_read_b128 v[26:29], v2
	ds_read_b128 v[30:33], v2 offset:1024
	ds_read_b128 v[18:21], v2 offset:2048
	ds_read_b128 v[22:25], v2 offset:3072
	ds_read_b128 v[10:13], v6
	ds_read_b128 v[14:17], v6 offset:1024
	ds_read_b128 v[2:5], v6 offset:2048
	ds_read_b128 v[6:9], v6 offset:3072
	v_lshl_add_u64 v[214:215], v[168:169], 0, s[6:7]
	s_add_i32 m0, s64, 0xc000
	ds_read_b128 v[172:175], v189
	ds_read_b128 v[176:179], v189 offset:1024
	ds_read_b128 v[190:193], v189 offset:2048
	ds_read_b128 v[194:197], v189 offset:3072
	ds_read_b128 v[198:201], v189 offset:4096
	ds_read_b128 v[202:205], v189 offset:5120
	ds_read_b128 v[206:209], v189 offset:6144
	ds_read_b128 v[210:213], v189 offset:7168
	global_load_lds_dwordx4 v[214:215], off
	v_lshl_add_u64 v[214:215], v[170:171], 0, s[6:7]
	s_add_i32 m0, s64, 0xe000
	s_nop 0
	global_load_lds_dwordx4 v[214:215], off
	s_waitcnt vmcnt(8)
	s_waitcnt lgkmcnt(0)
	s_barrier
	s_setprio 1
	s_waitcnt lgkmcnt(0)
	v_mfma_scale_f32_16x16x128_f8f6f4 v[158:161], v[26:33], v[172:179], v[158:161], v187, v187 op_sel_hi:[0,0,0]
	v_mfma_scale_f32_16x16x128_f8f6f4 v[154:157], v[18:25], v[172:179], v[154:157], v187, v187 op_sel_hi:[0,0,0]
	v_mfma_scale_f32_16x16x128_f8f6f4 v[118:121], v[18:25], v[190:197], v[118:121], v187, v187 op_sel_hi:[0,0,0]
	v_mfma_scale_f32_16x16x128_f8f6f4 v[122:125], v[26:33], v[190:197], v[122:125], v187, v187 op_sel_hi:[0,0,0]
	v_mfma_scale_f32_16x16x128_f8f6f4 v[126:129], v[26:33], v[198:205], v[126:129], v187, v187 op_sel_hi:[0,0,0]
	v_mfma_scale_f32_16x16x128_f8f6f4 v[114:117], v[18:25], v[198:205], v[114:117], v187, v187 op_sel_hi:[0,0,0]
	v_mfma_scale_f32_16x16x128_f8f6f4 v[106:109], v[18:25], v[206:213], v[106:109], v187, v187 op_sel_hi:[0,0,0]
	v_mfma_scale_f32_16x16x128_f8f6f4 v[110:113], v[26:33], v[206:213], v[110:113], v187, v187 op_sel_hi:[0,0,0]
	s_setprio 0
	s_setprio 1
	v_mfma_scale_f32_16x16x128_f8f6f4 v[102:105], v[10:17], v[206:213], v[102:105], v187, v187 op_sel_hi:[0,0,0]
	v_mfma_scale_f32_16x16x128_f8f6f4 v[98:101], v[2:9], v[206:213], v[98:101], v187, v187 op_sel_hi:[0,0,0]
	v_mfma_scale_f32_16x16x128_f8f6f4 v[130:133], v[2:9], v[198:205], v[130:133], v187, v187 op_sel_hi:[0,0,0]
	v_mfma_scale_f32_16x16x128_f8f6f4 v[134:137], v[10:17], v[198:205], v[134:137], v187, v187 op_sel_hi:[0,0,0]
	v_mfma_scale_f32_16x16x128_f8f6f4 v[142:145], v[10:17], v[190:197], v[142:145], v187, v187 op_sel_hi:[0,0,0]
	v_mfma_scale_f32_16x16x128_f8f6f4 v[138:141], v[2:9], v[190:197], v[138:141], v187, v187 op_sel_hi:[0,0,0]
	v_mfma_scale_f32_16x16x128_f8f6f4 v[146:149], v[2:9], v[172:179], v[146:149], v187, v187 op_sel_hi:[0,0,0]
	v_mfma_scale_f32_16x16x128_f8f6f4 v[150:153], v[10:17], v[172:179], v[150:153], v187, v187 op_sel_hi:[0,0,0]
	s_setprio 0
	s_barrier
	s_add_i32 s72, s72, s43
	v_lshl_add_u64 v[172:173], s[8:9], 0, v[162:163]
	s_mov_b32 m0, s72
	ds_read_b128 v[190:193], v189 offset:16384
	ds_read_b128 v[194:197], v189 offset:17408
	ds_read_b128 v[198:201], v189 offset:18432
	ds_read_b128 v[202:205], v189 offset:19456
	ds_read_b128 v[206:209], v189 offset:20480
	ds_read_b128 v[210:213], v189 offset:21504
	ds_read_b128 v[214:217], v189 offset:22528
	ds_read_b128 v[218:221], v189 offset:23552
	global_load_lds_dwordx4 v[172:173], off
	s_add_i32 m0, s72, 0x2000
	s_add_u32 s74, s8, 0x158000
	v_lshl_add_u64 v[174:175], s[8:9], 0, v[166:167]
	s_addc_u32 s75, s9, 0
	s_add_i32 s72, s73, s43
	global_load_lds_dwordx4 v[174:175], off
	v_lshl_add_u64 v[176:177], s[74:75], 0, v[162:163]
	s_mov_b32 m0, s72
	v_lshl_add_u64 v[178:179], s[36:37], 0, v[166:167]
	global_load_lds_dwordx4 v[176:177], off
	v_lshl_add_u64 v[176:177], s[74:75], 0, v[166:167]
	s_add_i32 m0, s72, 0x2000
	s_nop 0
	global_load_lds_dwordx4 v[176:177], off
	v_lshl_add_u64 v[176:177], s[36:37], 0, v[162:163]
	s_mov_b32 m0, s64
	s_nop 0
	global_load_lds_dwordx4 v[176:177], off
	s_mov_b32 m0, s65
	s_nop 0
	global_load_lds_dwordx4 v[178:179], off
	s_waitcnt vmcnt(8)
	s_waitcnt lgkmcnt(0)
	s_barrier
	s_setprio 1
	s_waitcnt lgkmcnt(0)
	v_mfma_scale_f32_16x16x128_f8f6f4 v[94:97], v[26:33], v[190:197], v[94:97], v187, v187 op_sel_hi:[0,0,0]
	v_mfma_scale_f32_16x16x128_f8f6f4 v[90:93], v[18:25], v[190:197], v[90:93], v187, v187 op_sel_hi:[0,0,0]
	v_mfma_scale_f32_16x16x128_f8f6f4 v[74:77], v[18:25], v[198:205], v[74:77], v187, v187 op_sel_hi:[0,0,0]
	v_mfma_scale_f32_16x16x128_f8f6f4 v[78:81], v[26:33], v[198:205], v[78:81], v187, v187 op_sel_hi:[0,0,0]
	v_mfma_scale_f32_16x16x128_f8f6f4 v[62:65], v[26:33], v[206:213], v[62:65], v187, v187 op_sel_hi:[0,0,0]
	v_mfma_scale_f32_16x16x128_f8f6f4 v[58:61], v[18:25], v[206:213], v[58:61], v187, v187 op_sel_hi:[0,0,0]
	v_mfma_scale_f32_16x16x128_f8f6f4 v[42:45], v[18:25], v[214:221], v[42:45], v187, v187 op_sel_hi:[0,0,0]
	v_mfma_scale_f32_16x16x128_f8f6f4 v[46:49], v[26:33], v[214:221], v[46:49], v187, v187 op_sel_hi:[0,0,0]
	s_setprio 0
	s_setprio 1
	v_mfma_scale_f32_16x16x128_f8f6f4 v[38:41], v[10:17], v[214:221], v[38:41], v187, v187 op_sel_hi:[0,0,0]
	v_mfma_scale_f32_16x16x128_f8f6f4 v[34:37], v[2:9], v[214:221], v[34:37], v187, v187 op_sel_hi:[0,0,0]
	v_mfma_scale_f32_16x16x128_f8f6f4 v[50:53], v[2:9], v[206:213], v[50:53], v187, v187 op_sel_hi:[0,0,0]
	v_mfma_scale_f32_16x16x128_f8f6f4 v[54:57], v[10:17], v[206:213], v[54:57], v187, v187 op_sel_hi:[0,0,0]
	v_mfma_scale_f32_16x16x128_f8f6f4 v[70:73], v[10:17], v[198:205], v[70:73], v187, v187 op_sel_hi:[0,0,0]
	v_mfma_scale_f32_16x16x128_f8f6f4 v[66:69], v[2:9], v[198:205], v[66:69], v187, v187 op_sel_hi:[0,0,0]
	v_mfma_scale_f32_16x16x128_f8f6f4 v[82:85], v[2:9], v[190:197], v[82:85], v187, v187 op_sel_hi:[0,0,0]
	v_mfma_scale_f32_16x16x128_f8f6f4 v[86:89], v[10:17], v[190:197], v[86:89], v187, v187 op_sel_hi:[0,0,0]
	s_setprio 0
	s_barrier
	s_add_i32 s72, 0, 0x18000
	s_add_i32 s73, 0, 0x1c000
	v_add_u32_e32 v14, s72, v188
	v_add_u32_e32 v30, s73, v188
	ds_read_b128 v[2:5], v14
	ds_read_b128 v[6:9], v14 offset:1024
	ds_read_b128 v[10:13], v14 offset:2048
	ds_read_b128 v[14:17], v14 offset:3072
	ds_read_b128 v[18:21], v30
	ds_read_b128 v[22:25], v30 offset:1024
	ds_read_b128 v[26:29], v30 offset:2048
	ds_read_b128 v[30:33], v30 offset:3072
	s_add_u32 s36, s36, 0x158000
	s_addc_u32 s37, s37, 0
	s_mov_b32 m0, s66
	v_lshl_add_u64 v[222:223], s[36:37], 0, v[162:163]
	ds_read_b128 v[190:193], v189 offset:32768
	ds_read_b128 v[194:197], v189 offset:33792
	ds_read_b128 v[198:201], v189 offset:34816
	ds_read_b128 v[202:205], v189 offset:35840
	ds_read_b128 v[206:209], v189 offset:36864
	ds_read_b128 v[210:213], v189 offset:37888
	ds_read_b128 v[214:217], v189 offset:38912
	ds_read_b128 v[218:221], v189 offset:39936
	global_load_lds_dwordx4 v[222:223], off
	v_lshl_add_u64 v[222:223], s[36:37], 0, v[166:167]
	s_mov_b32 m0, s67
	s_nop 0
	global_load_lds_dwordx4 v[222:223], off
	s_waitcnt vmcnt(8)
	s_waitcnt lgkmcnt(0)
	s_barrier
	s_setprio 1
	s_waitcnt lgkmcnt(0)
	v_mfma_scale_f32_16x16x128_f8f6f4 v[158:161], v[2:9], v[190:197], v[158:161], v187, v187 op_sel_hi:[0,0,0]
	v_mfma_scale_f32_16x16x128_f8f6f4 v[154:157], v[10:17], v[190:197], v[154:157], v187, v187 op_sel_hi:[0,0,0]
	v_mfma_scale_f32_16x16x128_f8f6f4 v[118:121], v[10:17], v[198:205], v[118:121], v187, v187 op_sel_hi:[0,0,0]
	v_mfma_scale_f32_16x16x128_f8f6f4 v[122:125], v[2:9], v[198:205], v[122:125], v187, v187 op_sel_hi:[0,0,0]
	v_mfma_scale_f32_16x16x128_f8f6f4 v[126:129], v[2:9], v[206:213], v[126:129], v187, v187 op_sel_hi:[0,0,0]
	v_mfma_scale_f32_16x16x128_f8f6f4 v[114:117], v[10:17], v[206:213], v[114:117], v187, v187 op_sel_hi:[0,0,0]
	v_mfma_scale_f32_16x16x128_f8f6f4 v[106:109], v[10:17], v[214:221], v[106:109], v187, v187 op_sel_hi:[0,0,0]
	v_mfma_scale_f32_16x16x128_f8f6f4 v[110:113], v[2:9], v[214:221], v[110:113], v187, v187 op_sel_hi:[0,0,0]
	s_setprio 0
	s_setprio 1
	v_mfma_scale_f32_16x16x128_f8f6f4 v[102:105], v[18:25], v[214:221], v[102:105], v187, v187 op_sel_hi:[0,0,0]
	v_mfma_scale_f32_16x16x128_f8f6f4 v[98:101], v[26:33], v[214:221], v[98:101], v187, v187 op_sel_hi:[0,0,0]
	v_mfma_scale_f32_16x16x128_f8f6f4 v[130:133], v[26:33], v[206:213], v[130:133], v187, v187 op_sel_hi:[0,0,0]
	v_mfma_scale_f32_16x16x128_f8f6f4 v[134:137], v[18:25], v[206:213], v[134:137], v187, v187 op_sel_hi:[0,0,0]
	v_mfma_scale_f32_16x16x128_f8f6f4 v[142:145], v[18:25], v[198:205], v[142:145], v187, v187 op_sel_hi:[0,0,0]
	v_mfma_scale_f32_16x16x128_f8f6f4 v[138:141], v[26:33], v[198:205], v[138:141], v187, v187 op_sel_hi:[0,0,0]
	v_mfma_scale_f32_16x16x128_f8f6f4 v[146:149], v[26:33], v[190:197], v[146:149], v187, v187 op_sel_hi:[0,0,0]
	v_mfma_scale_f32_16x16x128_f8f6f4 v[150:153], v[18:25], v[190:197], v[150:153], v187, v187 op_sel_hi:[0,0,0]
	s_setprio 0
	s_barrier
	s_add_i32 s36, s72, s43
	v_lshl_add_u64 v[172:173], v[172:173], 0, s[22:23]
	s_mov_b32 m0, s36
	ds_read_b128 v[190:193], v189 offset:49152
	ds_read_b128 v[194:197], v189 offset:50176
	ds_read_b128 v[198:201], v189 offset:51200
	ds_read_b128 v[202:205], v189 offset:52224
	ds_read_b128 v[206:209], v189 offset:53248
	ds_read_b128 v[210:213], v189 offset:54272
	ds_read_b128 v[214:217], v189 offset:55296
	ds_read_b128 v[218:221], v189 offset:56320
	global_load_lds_dwordx4 v[172:173], off
	s_add_i32 m0, s36, 0x2000
	s_add_u32 s8, s8, 0x158080
	v_lshl_add_u64 v[172:173], v[174:175], 0, s[22:23]
	s_addc_u32 s9, s9, 0
	s_add_i32 s36, s73, s43
	global_load_lds_dwordx4 v[172:173], off
	v_lshl_add_u64 v[172:173], s[8:9], 0, v[162:163]
	s_mov_b32 m0, s36
	s_nop 0
	global_load_lds_dwordx4 v[172:173], off
	v_lshl_add_u64 v[172:173], s[8:9], 0, v[166:167]
	s_add_i32 m0, s36, 0x2000
	s_nop 0
	global_load_lds_dwordx4 v[172:173], off
	v_lshl_add_u64 v[172:173], v[176:177], 0, s[22:23]
	s_mov_b32 m0, s69
	s_nop 0
	global_load_lds_dwordx4 v[172:173], off
	v_lshl_add_u64 v[172:173], v[178:179], 0, s[22:23]
	s_mov_b32 m0, s70
	s_nop 0
	global_load_lds_dwordx4 v[172:173], off
	s_waitcnt vmcnt(8)
	s_waitcnt lgkmcnt(0)
	s_barrier
	s_setprio 1
	s_waitcnt lgkmcnt(0)
	v_mfma_scale_f32_16x16x128_f8f6f4 v[94:97], v[2:9], v[190:197], v[94:97], v187, v187 op_sel_hi:[0,0,0]
	v_mfma_scale_f32_16x16x128_f8f6f4 v[90:93], v[10:17], v[190:197], v[90:93], v187, v187 op_sel_hi:[0,0,0]
	v_mfma_scale_f32_16x16x128_f8f6f4 v[74:77], v[10:17], v[198:205], v[74:77], v187, v187 op_sel_hi:[0,0,0]
	v_mfma_scale_f32_16x16x128_f8f6f4 v[78:81], v[2:9], v[198:205], v[78:81], v187, v187 op_sel_hi:[0,0,0]
	v_mfma_scale_f32_16x16x128_f8f6f4 v[62:65], v[2:9], v[206:213], v[62:65], v187, v187 op_sel_hi:[0,0,0]
	v_mfma_scale_f32_16x16x128_f8f6f4 v[58:61], v[10:17], v[206:213], v[58:61], v187, v187 op_sel_hi:[0,0,0]
	v_mfma_scale_f32_16x16x128_f8f6f4 v[42:45], v[10:17], v[214:221], v[42:45], v187, v187 op_sel_hi:[0,0,0]
	v_mfma_scale_f32_16x16x128_f8f6f4 v[46:49], v[2:9], v[214:221], v[46:49], v187, v187 op_sel_hi:[0,0,0]
	s_setprio 0
	s_setprio 1
	v_mfma_scale_f32_16x16x128_f8f6f4 v[38:41], v[18:25], v[214:221], v[38:41], v187, v187 op_sel_hi:[0,0,0]
	v_mfma_scale_f32_16x16x128_f8f6f4 v[34:37], v[26:33], v[214:221], v[34:37], v187, v187 op_sel_hi:[0,0,0]
	v_mfma_scale_f32_16x16x128_f8f6f4 v[50:53], v[26:33], v[206:213], v[50:53], v187, v187 op_sel_hi:[0,0,0]
	v_mfma_scale_f32_16x16x128_f8f6f4 v[54:57], v[18:25], v[206:213], v[54:57], v187, v187 op_sel_hi:[0,0,0]
	v_mfma_scale_f32_16x16x128_f8f6f4 v[70:73], v[18:25], v[198:205], v[70:73], v187, v187 op_sel_hi:[0,0,0]
	v_mfma_scale_f32_16x16x128_f8f6f4 v[66:69], v[26:33], v[198:205], v[66:69], v187, v187 op_sel_hi:[0,0,0]
	v_mfma_scale_f32_16x16x128_f8f6f4 v[82:85], v[26:33], v[190:197], v[82:85], v187, v187 op_sel_hi:[0,0,0]
	v_mfma_scale_f32_16x16x128_f8f6f4 v[86:89], v[18:25], v[190:197], v[86:89], v187, v187 op_sel_hi:[0,0,0]
	s_setprio 0
	s_barrier
	s_add_i32 s71, s71, 2
	s_add_u32 s6, s6, 0x100
	s_addc_u32 s7, s7, 0
	s_cmpk_lt_u32 s71, 0x54
	s_cbranch_scc1 .LBB0_1745
	s_waitcnt vmcnt(0)
	s_cmpk_gt_u32 s40, 0xff
	s_cbranch_scc1 .LBB0_1748
	s_barrier

.LBB0_1807:
	ds_read_b128 v[26:29], v185
	ds_read_b128 v[30:33], v185 offset:1024
	ds_read_b128 v[18:21], v185 offset:2048
	ds_read_b128 v[22:25], v185 offset:3072
	ds_read_b128 v[10:13], v186
	ds_read_b128 v[14:17], v186 offset:1024
	ds_read_b128 v[2:5], v186 offset:2048
	ds_read_b128 v[6:9], v186 offset:3072
	s_add_u32 s28, s26, 0xffea8080
	s_addc_u32 s29, s27, -1
	s_cmpk_eq_i32 s58, 0x52
	s_cselect_b32 s31, s5, s29
	s_cselect_b32 s30, s4, s28
	s_cselect_b32 s29, s25, s57
	s_cselect_b32 s28, s24, s56
	v_lshl_add_u64 v[212:213], s[26:27], 0, v[166:167]
	s_add_i32 m0, s34, 0xc000
	ds_read_b128 v[174:177], v187
	ds_read_b128 v[178:181], v187 offset:1024
	ds_read_b128 v[188:191], v187 offset:2048
	ds_read_b128 v[192:195], v187 offset:3072
	ds_read_b128 v[196:199], v187 offset:4096
	ds_read_b128 v[200:203], v187 offset:5120
	ds_read_b128 v[204:207], v187 offset:6144
	ds_read_b128 v[208:211], v187 offset:7168
	global_load_lds_dwordx4 v[212:213], off
	v_lshl_add_u64 v[212:213], s[26:27], 0, v[168:169]
	s_add_i32 m0, s34, 0xe000
	s_nop 0
	global_load_lds_dwordx4 v[212:213], off
	s_waitcnt vmcnt(8)
	s_waitcnt lgkmcnt(0)
	s_barrier
	s_setprio 1
	s_waitcnt lgkmcnt(0)
	v_mfma_scale_f32_16x16x128_f8f6f4 v[158:161], v[26:33], v[174:181], v[158:161], v1, v1 op_sel_hi:[0,0,0]
	v_mfma_scale_f32_16x16x128_f8f6f4 v[154:157], v[18:25], v[174:181], v[154:157], v1, v1 op_sel_hi:[0,0,0]
	v_mfma_scale_f32_16x16x128_f8f6f4 v[138:141], v[18:25], v[188:195], v[138:141], v1, v1 op_sel_hi:[0,0,0]
	v_mfma_scale_f32_16x16x128_f8f6f4 v[142:145], v[26:33], v[188:195], v[142:145], v1, v1 op_sel_hi:[0,0,0]
	v_mfma_scale_f32_16x16x128_f8f6f4 v[126:129], v[26:33], v[196:203], v[126:129], v1, v1 op_sel_hi:[0,0,0]
	v_mfma_scale_f32_16x16x128_f8f6f4 v[122:125], v[18:25], v[196:203], v[122:125], v1, v1 op_sel_hi:[0,0,0]
	v_mfma_scale_f32_16x16x128_f8f6f4 v[106:109], v[18:25], v[204:211], v[106:109], v1, v1 op_sel_hi:[0,0,0]
	v_mfma_scale_f32_16x16x128_f8f6f4 v[110:113], v[26:33], v[204:211], v[110:113], v1, v1 op_sel_hi:[0,0,0]
	s_setprio 0
	s_setprio 1
	v_mfma_scale_f32_16x16x128_f8f6f4 v[102:105], v[10:17], v[204:211], v[102:105], v1, v1 op_sel_hi:[0,0,0]
	v_mfma_scale_f32_16x16x128_f8f6f4 v[98:101], v[2:9], v[204:211], v[98:101], v1, v1 op_sel_hi:[0,0,0]
	v_mfma_scale_f32_16x16x128_f8f6f4 v[114:117], v[2:9], v[196:203], v[114:117], v1, v1 op_sel_hi:[0,0,0]
	v_mfma_scale_f32_16x16x128_f8f6f4 v[118:121], v[10:17], v[196:203], v[118:121], v1, v1 op_sel_hi:[0,0,0]
	v_mfma_scale_f32_16x16x128_f8f6f4 v[134:137], v[10:17], v[188:195], v[134:137], v1, v1 op_sel_hi:[0,0,0]
	v_mfma_scale_f32_16x16x128_f8f6f4 v[130:133], v[2:9], v[188:195], v[130:133], v1, v1 op_sel_hi:[0,0,0]
	v_mfma_scale_f32_16x16x128_f8f6f4 v[146:149], v[2:9], v[174:181], v[146:149], v1, v1 op_sel_hi:[0,0,0]
	v_mfma_scale_f32_16x16x128_f8f6f4 v[150:153], v[10:17], v[174:181], v[150:153], v1, v1 op_sel_hi:[0,0,0]
	s_setprio 0
	s_barrier
	s_add_i32 s59, s42, s3
	v_lshl_add_u64 v[174:175], s[28:29], 0, v[164:165]
	s_mov_b32 m0, s59
	ds_read_b128 v[188:191], v187 offset:16384
	ds_read_b128 v[192:195], v187 offset:17408
	ds_read_b128 v[196:199], v187 offset:18432
	ds_read_b128 v[200:203], v187 offset:19456
	ds_read_b128 v[204:207], v187 offset:20480
	ds_read_b128 v[208:211], v187 offset:21504
	ds_read_b128 v[212:215], v187 offset:22528
	ds_read_b128 v[216:219], v187 offset:23552
	global_load_lds_dwordx4 v[174:175], off
	s_add_i32 m0, s59, 0x2000
	s_add_u32 s60, s28, 0x158000
	v_lshl_add_u64 v[176:177], s[28:29], 0, v[162:163]
	s_addc_u32 s61, s29, 0
	s_add_i32 s59, s43, s3
	global_load_lds_dwordx4 v[176:177], off
	v_lshl_add_u64 v[178:179], s[60:61], 0, v[164:165]
	s_mov_b32 m0, s59
	v_lshl_add_u64 v[180:181], s[30:31], 0, v[162:163]
	global_load_lds_dwordx4 v[178:179], off
	v_lshl_add_u64 v[178:179], s[60:61], 0, v[162:163]
	s_add_i32 m0, s59, 0x2000
	s_nop 0
	global_load_lds_dwordx4 v[178:179], off
	v_lshl_add_u64 v[178:179], s[30:31], 0, v[164:165]
	s_mov_b32 m0, s34
	s_nop 0
	global_load_lds_dwordx4 v[178:179], off
	s_mov_b32 m0, s35
	s_nop 0
	global_load_lds_dwordx4 v[180:181], off
	s_waitcnt vmcnt(8)
	s_waitcnt lgkmcnt(0)
	s_barrier
	s_setprio 1
	s_waitcnt lgkmcnt(0)
	v_mfma_scale_f32_16x16x128_f8f6f4 v[94:97], v[26:33], v[188:195], v[94:97], v1, v1 op_sel_hi:[0,0,0]
	v_mfma_scale_f32_16x16x128_f8f6f4 v[90:93], v[18:25], v[188:195], v[90:93], v1, v1 op_sel_hi:[0,0,0]
	v_mfma_scale_f32_16x16x128_f8f6f4 v[74:77], v[18:25], v[196:203], v[74:77], v1, v1 op_sel_hi:[0,0,0]
	v_mfma_scale_f32_16x16x128_f8f6f4 v[78:81], v[26:33], v[196:203], v[78:81], v1, v1 op_sel_hi:[0,0,0]
	v_mfma_scale_f32_16x16x128_f8f6f4 v[62:65], v[26:33], v[204:211], v[62:65], v1, v1 op_sel_hi:[0,0,0]
	v_mfma_scale_f32_16x16x128_f8f6f4 v[58:61], v[18:25], v[204:211], v[58:61], v1, v1 op_sel_hi:[0,0,0]
	v_mfma_scale_f32_16x16x128_f8f6f4 v[42:45], v[18:25], v[212:219], v[42:45], v1, v1 op_sel_hi:[0,0,0]
	v_mfma_scale_f32_16x16x128_f8f6f4 v[54:57], v[26:33], v[212:219], v[54:57], v1, v1 op_sel_hi:[0,0,0]
	s_setprio 0
	s_setprio 1
	v_mfma_scale_f32_16x16x128_f8f6f4 v[38:41], v[10:17], v[212:219], v[38:41], v1, v1 op_sel_hi:[0,0,0]
	v_mfma_scale_f32_16x16x128_f8f6f4 v[34:37], v[2:9], v[212:219], v[34:37], v1, v1 op_sel_hi:[0,0,0]
	v_mfma_scale_f32_16x16x128_f8f6f4 v[46:49], v[2:9], v[204:211], v[46:49], v1, v1 op_sel_hi:[0,0,0]
	v_mfma_scale_f32_16x16x128_f8f6f4 v[50:53], v[10:17], v[204:211], v[50:53], v1, v1 op_sel_hi:[0,0,0]
	v_mfma_scale_f32_16x16x128_f8f6f4 v[70:73], v[10:17], v[196:203], v[70:73], v1, v1 op_sel_hi:[0,0,0]
	v_mfma_scale_f32_16x16x128_f8f6f4 v[66:69], v[2:9], v[196:203], v[66:69], v1, v1 op_sel_hi:[0,0,0]
	v_mfma_scale_f32_16x16x128_f8f6f4 v[82:85], v[2:9], v[188:195], v[82:85], v1, v1 op_sel_hi:[0,0,0]
	v_mfma_scale_f32_16x16x128_f8f6f4 v[86:89], v[10:17], v[188:195], v[86:89], v1, v1 op_sel_hi:[0,0,0]
	s_setprio 0
	s_barrier
	s_add_i32 s59, 0, 0x18000
	s_add_i32 s60, 0, 0x1c000
	v_add_u32_e32 v14, s59, v183
	v_add_u32_e32 v30, s60, v183
	ds_read_b128 v[2:5], v14
	ds_read_b128 v[6:9], v14 offset:1024
	ds_read_b128 v[10:13], v14 offset:2048
	ds_read_b128 v[14:17], v14 offset:3072
	ds_read_b128 v[18:21], v30
	ds_read_b128 v[22:25], v30 offset:1024
	ds_read_b128 v[26:29], v30 offset:2048
	ds_read_b128 v[30:33], v30 offset:3072
	s_add_u32 s30, s30, 0x158000
	s_addc_u32 s31, s31, 0
	s_mov_b32 m0, s36
	v_lshl_add_u64 v[220:221], s[30:31], 0, v[164:165]
	ds_read_b128 v[188:191], v187 offset:32768
	ds_read_b128 v[192:195], v187 offset:33792
	ds_read_b128 v[196:199], v187 offset:34816
	ds_read_b128 v[200:203], v187 offset:35840
	ds_read_b128 v[204:207], v187 offset:36864
	ds_read_b128 v[208:211], v187 offset:37888
	ds_read_b128 v[212:215], v187 offset:38912
	ds_read_b128 v[216:219], v187 offset:39936
	global_load_lds_dwordx4 v[220:221], off
	v_lshl_add_u64 v[220:221], s[30:31], 0, v[162:163]
	s_mov_b32 m0, s37
	s_nop 0
	global_load_lds_dwordx4 v[220:221], off
	s_waitcnt vmcnt(8)
	s_waitcnt lgkmcnt(0)
	s_barrier
	s_setprio 1
	s_waitcnt lgkmcnt(0)
	v_mfma_scale_f32_16x16x128_f8f6f4 v[158:161], v[2:9], v[188:195], v[158:161], v1, v1 op_sel_hi:[0,0,0]
	v_mfma_scale_f32_16x16x128_f8f6f4 v[154:157], v[10:17], v[188:195], v[154:157], v1, v1 op_sel_hi:[0,0,0]
	v_mfma_scale_f32_16x16x128_f8f6f4 v[138:141], v[10:17], v[196:203], v[138:141], v1, v1 op_sel_hi:[0,0,0]
	v_mfma_scale_f32_16x16x128_f8f6f4 v[142:145], v[2:9], v[196:203], v[142:145], v1, v1 op_sel_hi:[0,0,0]
	v_mfma_scale_f32_16x16x128_f8f6f4 v[126:129], v[2:9], v[204:211], v[126:129], v1, v1 op_sel_hi:[0,0,0]
	v_mfma_scale_f32_16x16x128_f8f6f4 v[122:125], v[10:17], v[204:211], v[122:125], v1, v1 op_sel_hi:[0,0,0]
	v_mfma_scale_f32_16x16x128_f8f6f4 v[106:109], v[10:17], v[212:219], v[106:109], v1, v1 op_sel_hi:[0,0,0]
	v_mfma_scale_f32_16x16x128_f8f6f4 v[110:113], v[2:9], v[212:219], v[110:113], v1, v1 op_sel_hi:[0,0,0]
	s_setprio 0
	s_setprio 1
	v_mfma_scale_f32_16x16x128_f8f6f4 v[102:105], v[18:25], v[212:219], v[102:105], v1, v1 op_sel_hi:[0,0,0]
	v_mfma_scale_f32_16x16x128_f8f6f4 v[98:101], v[26:33], v[212:219], v[98:101], v1, v1 op_sel_hi:[0,0,0]
	v_mfma_scale_f32_16x16x128_f8f6f4 v[114:117], v[26:33], v[204:211], v[114:117], v1, v1 op_sel_hi:[0,0,0]
	v_mfma_scale_f32_16x16x128_f8f6f4 v[118:121], v[18:25], v[204:211], v[118:121], v1, v1 op_sel_hi:[0,0,0]
	v_mfma_scale_f32_16x16x128_f8f6f4 v[134:137], v[18:25], v[196:203], v[134:137], v1, v1 op_sel_hi:[0,0,0]
	v_mfma_scale_f32_16x16x128_f8f6f4 v[130:133], v[26:33], v[196:203], v[130:133], v1, v1 op_sel_hi:[0,0,0]
	v_mfma_scale_f32_16x16x128_f8f6f4 v[146:149], v[26:33], v[188:195], v[146:149], v1, v1 op_sel_hi:[0,0,0]
	v_mfma_scale_f32_16x16x128_f8f6f4 v[150:153], v[18:25], v[188:195], v[150:153], v1, v1 op_sel_hi:[0,0,0]
	s_setprio 0
	s_barrier
	s_add_i32 s30, s59, s3
	v_lshl_add_u64 v[174:175], v[174:175], 0, s[10:11]
	s_mov_b32 m0, s30
	ds_read_b128 v[188:191], v187 offset:49152
	ds_read_b128 v[192:195], v187 offset:50176
	ds_read_b128 v[196:199], v187 offset:51200
	ds_read_b128 v[200:203], v187 offset:52224
	ds_read_b128 v[204:207], v187 offset:53248
	ds_read_b128 v[208:211], v187 offset:54272
	ds_read_b128 v[212:215], v187 offset:55296
	ds_read_b128 v[216:219], v187 offset:56320
	global_load_lds_dwordx4 v[174:175], off
	s_add_i32 m0, s30, 0x2000
	s_add_u32 s28, s28, 0x158080
	v_lshl_add_u64 v[174:175], v[176:177], 0, s[10:11]
	s_addc_u32 s29, s29, 0
	s_add_i32 s30, s60, s3
	global_load_lds_dwordx4 v[174:175], off
	v_lshl_add_u64 v[174:175], s[28:29], 0, v[164:165]
	s_mov_b32 m0, s30
	s_nop 0
	global_load_lds_dwordx4 v[174:175], off
	v_lshl_add_u64 v[174:175], s[28:29], 0, v[162:163]
	s_add_i32 m0, s30, 0x2000
	s_nop 0
	global_load_lds_dwordx4 v[174:175], off
	v_lshl_add_u64 v[174:175], v[178:179], 0, s[10:11]
	s_mov_b32 m0, s40
	s_nop 0
	global_load_lds_dwordx4 v[174:175], off
	v_lshl_add_u64 v[174:175], v[180:181], 0, s[10:11]
	s_mov_b32 m0, s41
	s_nop 0
	global_load_lds_dwordx4 v[174:175], off
	s_waitcnt vmcnt(8)
	s_waitcnt lgkmcnt(0)
	s_barrier
	s_setprio 1
	s_waitcnt lgkmcnt(0)
	v_mfma_scale_f32_16x16x128_f8f6f4 v[94:97], v[2:9], v[188:195], v[94:97], v1, v1 op_sel_hi:[0,0,0]
	v_mfma_scale_f32_16x16x128_f8f6f4 v[90:93], v[10:17], v[188:195], v[90:93], v1, v1 op_sel_hi:[0,0,0]
	v_mfma_scale_f32_16x16x128_f8f6f4 v[74:77], v[10:17], v[196:203], v[74:77], v1, v1 op_sel_hi:[0,0,0]
	v_mfma_scale_f32_16x16x128_f8f6f4 v[78:81], v[2:9], v[196:203], v[78:81], v1, v1 op_sel_hi:[0,0,0]
	v_mfma_scale_f32_16x16x128_f8f6f4 v[62:65], v[2:9], v[204:211], v[62:65], v1, v1 op_sel_hi:[0,0,0]
	v_mfma_scale_f32_16x16x128_f8f6f4 v[58:61], v[10:17], v[204:211], v[58:61], v1, v1 op_sel_hi:[0,0,0]
	v_mfma_scale_f32_16x16x128_f8f6f4 v[42:45], v[10:17], v[212:219], v[42:45], v1, v1 op_sel_hi:[0,0,0]
	v_mfma_scale_f32_16x16x128_f8f6f4 v[54:57], v[2:9], v[212:219], v[54:57], v1, v1 op_sel_hi:[0,0,0]
	s_setprio 0
	s_setprio 1
	v_mfma_scale_f32_16x16x128_f8f6f4 v[38:41], v[18:25], v[212:219], v[38:41], v1, v1 op_sel_hi:[0,0,0]
	v_mfma_scale_f32_16x16x128_f8f6f4 v[34:37], v[26:33], v[212:219], v[34:37], v1, v1 op_sel_hi:[0,0,0]
	v_mfma_scale_f32_16x16x128_f8f6f4 v[46:49], v[26:33], v[204:211], v[46:49], v1, v1 op_sel_hi:[0,0,0]
	v_mfma_scale_f32_16x16x128_f8f6f4 v[50:53], v[18:25], v[204:211], v[50:53], v1, v1 op_sel_hi:[0,0,0]
	v_mfma_scale_f32_16x16x128_f8f6f4 v[70:73], v[18:25], v[196:203], v[70:73], v1, v1 op_sel_hi:[0,0,0]
	v_mfma_scale_f32_16x16x128_f8f6f4 v[66:69], v[26:33], v[196:203], v[66:69], v1, v1 op_sel_hi:[0,0,0]
	v_mfma_scale_f32_16x16x128_f8f6f4 v[82:85], v[26:33], v[188:195], v[82:85], v1, v1 op_sel_hi:[0,0,0]
	v_mfma_scale_f32_16x16x128_f8f6f4 v[86:89], v[18:25], v[188:195], v[86:89], v1, v1 op_sel_hi:[0,0,0]
	s_setprio 0
	s_barrier
	s_add_i32 s58, s58, 2
	s_add_u32 s26, s26, 0x100
	s_addc_u32 s27, s27, 0
	s_add_u32 s56, s56, 0x100
	s_addc_u32 s57, s57, 0
	s_cmpk_gt_u32 s58, 0x53
	s_cbranch_scc0 .LBB0_1807
	s_and_b64 vcc, exec, s[12:13]
	s_cbranch_vccz .LBB0_1810
	s_barrier
